# stack14 plus GEMM epilogue VALU trimming (E2 gate pre-scaled by 64, E1 x4 carried by the reciprocal, zero-inits before cvt_pk_fp8 dropped; bit-exact) and K-loop counter SALU moved in front of the loop
# speedup vs baseline: 1.0011x; 1.0008x over previous
; #define PG8_STAGE(bufoff, gbase, voff) do { const char* sb_ = (gbase); _Pragma("unroll") for (int _i = 0; _i < 2; ++_i) PG8_GLDS(sb_, (voff)[_i], bufoff, _i); } while (0)
; #define PG8_LDA(dst, b, h) do { if constexpr (F8) { _Pragma("unroll") for (int m = 0; m < 4; ++m) dst##8[m] = PG8_RD8(lds + PG8_SA(b, h) + aoff + m * 2048); } else { \
;         _Pragma("unroll") for (int m = 0; m < 4; ++m) _Pragma("unroll") for (int k = 0; k < 2; ++k) dst[m][k] = *(const PG8_LAS bf16x8*)(lds + PG8_SA(b, h) + aoff + m * 2048 + k * 1024); } } while (0)
; #define PG8_LDB(dst, b, h) do { if constexpr (F8) { _Pragma("unroll") for (int n = 0; n < 2; ++n) dst##8[n] = PG8_RD8(lds + PG8_SB(b, h) + boff + n * 2048); } else { \
;         _Pragma("unroll") for (int n = 0; n < 2; ++n) _Pragma("unroll") for (int k = 0; k < 2; ++k) dst[n][k] = *(const PG8_LAS bf16x8*)(lds + PG8_SB(b, h) + boff + n * 2048 + k * 1024); } } while (0)
; #define PG8_WAIT_V(n) asm volatile("s_waitcnt vmcnt(" #n ")" ::: "memory")
; #define PG8_WAIT_L(n) asm volatile("s_waitcnt lgkmcnt(" #n ")" ::: "memory")
; #define PG8_BAR __builtin_amdgcn_s_barrier()
; #define PG8_SCHED __builtin_amdgcn_sched_barrier(0)
;     ...
;         for (int t = 0; t < nt; t += 2) {
;             const bool last = (t == nt - 2);
;             const size_t k1 = (size_t)(t + 1) * kstep;
;             const size_t k2 = last ? 0 : (size_t)(t + 2) * kstep, k3 = k2 + kstep;
;             const char* b2 = last ? nB : cB + (size_t)(t + 2) * kstep; const char* b3 = b2 + kstep;
;             PG8_LDB(B0, 0, 0); PG8_LDB(B1, 0, 1); PG8_SCHED; PG8_LDA(At, 0, 0); PG8_STAGE_A(PG8_SA(1, 1), 1, k1, false);
;             PG8_WAIT_V(8); PG8_WAIT_L(0); PG8_BAR; PG8_MMA(0, 0, At, B0); PG8_MMA(0, 1, At, B1); PG8_BAR; PG8_SCHED;
;             PG8_LDA(At, 0, 1); PG8_STAGE(PG8_SB(0, 0), b2, voffB); PG8_STAGE(PG8_SB(0, 1), b2 + hstep, voffB); PG8_STAGE_A(PG8_SA(0, 0), 0, k2, last);
;             PG8_WAIT_V(8); PG8_WAIT_L(0); PG8_BAR; PG8_MMA(1, 0, At, B0); PG8_MMA(1, 1, At, B1); PG8_BAR; PG8_SCHED;
.LBB4_306:
	ds_read_b128 v[128:131], v212
	ds_read_b128 v[132:135], v212 offset:16
	ds_read_b128 v[136:139], v212 offset:2048
	ds_read_b128 v[140:143], v212 offset:2064
	ds_read_b128 v[144:147], v213
	ds_read_b128 v[148:151], v213 offset:16
	ds_read_b128 v[152:155], v213 offset:2048
	ds_read_b128 v[156:159], v213 offset:2064
	s_add_i32 s21, s26, 0xfffc0080
	s_add_u32 s28, s8, s26
	s_addc_u32 s29, s9, s27
	s_add_u32 s28, s28, 0xfffc0080
	s_addc_u32 s29, s29, -1
	s_add_u32 s30, s6, s26
	s_addc_u32 s31, s7, s27
	s_cmp_eq_u32 s19, 12
	s_cselect_b32 s21, 0, s21
	s_cselect_b32 s29, s25, s29
	s_cselect_b32 s28, s24, s28
	ds_read_b128 v[160:163], v214
	ds_read_b128 v[164:167], v214 offset:16
	ds_read_b128 v[168:171], v214 offset:2048
	ds_read_b128 v[172:175], v214 offset:2064
	ds_read_b128 v[176:179], v214 offset:4096
	ds_read_b128 v[180:183], v214 offset:4112
	ds_read_b128 v[184:187], v214 offset:6144
	ds_read_b128 v[188:191], v214 offset:6160
	s_mov_b32 m0, s75
	s_nop 0
	global_load_lds_dwordx4 v208, s[30:31]
	s_nop 0
	s_mov_b32 m0, s76
	s_nop 0
	global_load_lds_dwordx4 v210, s[30:31]
	s_waitcnt vmcnt(8)
	s_waitcnt lgkmcnt(0)
	s_barrier
	s_setprio 1
	v_mfma_scale_f32_16x16x128_f8f6f4 v[120:123], v[128:135], v[160:167], v[120:123], v216, v215 op_sel_hi:[0,0,0]
	v_mfma_scale_f32_16x16x128_f8f6f4 v[124:127], v[136:143], v[160:167], v[124:127], v216, v215 op_sel_hi:[0,0,0]
	v_mfma_scale_f32_16x16x128_f8f6f4 v[104:107], v[128:135], v[168:175], v[104:107], v216, v215 op_sel_hi:[0,0,0]
	v_mfma_scale_f32_16x16x128_f8f6f4 v[108:111], v[136:143], v[168:175], v[108:111], v216, v215 op_sel_hi:[0,0,0]
	v_mfma_scale_f32_16x16x128_f8f6f4 v[198:201], v[128:135], v[176:183], v[88:91], v216, v215 op_sel_hi:[0,0,0]
	v_mfma_scale_f32_16x16x128_f8f6f4 v[202:205], v[136:143], v[176:183], v[92:95], v216, v215 op_sel_hi:[0,0,0]
	v_mfma_scale_f32_16x16x128_f8f6f4 v[232:235], v[128:135], v[184:191], v[72:75], v216, v215 op_sel_hi:[0,0,0]
	v_mfma_scale_f32_16x16x128_f8f6f4 v[236:239], v[136:143], v[184:191], v[76:79], v216, v215 op_sel_hi:[0,0,0]
	s_setprio 0
	s_setprio 1
	v_mfma_scale_f32_16x16x128_f8f6f4 v[112:115], v[144:151], v[160:167], v[112:115], v216, v215 op_sel_hi:[0,0,0]
	v_mfma_scale_f32_16x16x128_f8f6f4 v[116:119], v[152:159], v[160:167], v[116:119], v216, v215 op_sel_hi:[0,0,0]
	v_mfma_scale_f32_16x16x128_f8f6f4 v[96:99], v[144:151], v[168:175], v[96:99], v216, v215 op_sel_hi:[0,0,0]
	v_mfma_scale_f32_16x16x128_f8f6f4 v[100:103], v[152:159], v[168:175], v[100:103], v216, v215 op_sel_hi:[0,0,0]
	v_mfma_scale_f32_16x16x128_f8f6f4 v[160:163], v[144:151], v[176:183], v[80:83], v216, v215 op_sel_hi:[0,0,0]
	v_mfma_scale_f32_16x16x128_f8f6f4 v[164:167], v[152:159], v[176:183], v[84:87], v216, v215 op_sel_hi:[0,0,0]
	v_mfma_scale_f32_16x16x128_f8f6f4 v[168:171], v[144:151], v[184:191], v[64:67], v216, v215 op_sel_hi:[0,0,0]
	v_mfma_scale_f32_16x16x128_f8f6f4 v[172:175], v[152:159], v[184:191], v[68:71], v216, v215 op_sel_hi:[0,0,0]
	s_setprio 0
	s_barrier
	s_nop 3
	ds_read_b128 v[64:67], v214 offset:16384
	ds_read_b128 v[68:71], v214 offset:16400
	ds_read_b128 v[72:75], v214 offset:18432
	ds_read_b128 v[76:79], v214 offset:18448
	ds_read_b128 v[80:83], v214 offset:20480
	ds_read_b128 v[84:87], v214 offset:20496
	ds_read_b128 v[88:91], v214 offset:22528
	ds_read_b128 v[92:95], v214 offset:22544
	s_mov_b32 m0, s43
	s_nop 0
	global_load_lds_dwordx4 v209, s[28:29]
	s_cselect_b32 s78, s23, s7
	s_mov_b32 m0, s54
	s_nop 0
	global_load_lds_dwordx4 v211, s[28:29]
	s_cselect_b32 s79, s22, s6
	s_add_u32 s30, s28, 0x40000
	s_addc_u32 s31, s29, 0
	s_mov_b32 m0, s55
	s_nop 0
	global_load_lds_dwordx4 v209, s[30:31]
	s_nop 0
	s_mov_b32 m0, s56
	s_nop 0
	global_load_lds_dwordx4 v211, s[30:31]
	s_add_u32 s30, s79, s21
	s_addc_u32 s31, s78, 0
	s_mov_b32 m0, s42
	s_nop 0
	global_load_lds_dwordx4 v208, s[30:31]
	s_nop 0
	s_mov_b32 m0, s57
	s_nop 0
	global_load_lds_dwordx4 v210, s[30:31]
	s_waitcnt vmcnt(8)
	s_waitcnt lgkmcnt(0)
	s_barrier
	s_setprio 1
	v_mfma_scale_f32_16x16x128_f8f6f4 v[56:59], v[128:135], v[64:71], v[56:59], v216, v215 op_sel_hi:[0,0,0]
	v_mfma_scale_f32_16x16x128_f8f6f4 v[60:63], v[136:143], v[64:71], v[60:63], v216, v215 op_sel_hi:[0,0,0]
	v_mfma_scale_f32_16x16x128_f8f6f4 v[8:11], v[128:135], v[88:95], v[8:11], v216, v215 op_sel_hi:[0,0,0]
	v_mfma_scale_f32_16x16x128_f8f6f4 v[176:179], v[128:135], v[72:79], v[40:43], v216, v215 op_sel_hi:[0,0,0]
	v_mfma_scale_f32_16x16x128_f8f6f4 v[180:183], v[136:143], v[72:79], v[44:47], v216, v215 op_sel_hi:[0,0,0]
	v_mfma_scale_f32_16x16x128_f8f6f4 v[184:187], v[128:135], v[80:87], v[24:27], v216, v215 op_sel_hi:[0,0,0]
	v_mfma_scale_f32_16x16x128_f8f6f4 v[188:191], v[136:143], v[80:87], v[28:31], v216, v215 op_sel_hi:[0,0,0]
	v_mfma_scale_f32_16x16x128_f8f6f4 v[240:243], v[136:143], v[88:95], v[12:15], v216, v215 op_sel_hi:[0,0,0]
	s_setprio 0
	s_setprio 1
	v_mfma_scale_f32_16x16x128_f8f6f4 v[52:55], v[152:159], v[64:71], v[52:55], v216, v215 op_sel_hi:[0,0,0]
	v_mfma_scale_f32_16x16x128_f8f6f4 v[244:247], v[144:151], v[64:71], v[48:51], v216, v215 op_sel_hi:[0,0,0]
	v_mfma_scale_f32_16x16x128_f8f6f4 v[248:251], v[144:151], v[72:79], v[32:35], v216, v215 op_sel_hi:[0,0,0]
	v_mfma_scale_f32_16x16x128_f8f6f4 v[252:255], v[152:159], v[72:79], v[36:39], v216, v215 op_sel_hi:[0,0,0]
	v_mfma_scale_f32_16x16x128_f8f6f4 v[224:227], v[144:151], v[80:87], v[16:19], v216, v215 op_sel_hi:[0,0,0]
	v_mfma_scale_f32_16x16x128_f8f6f4 v[192:195], v[152:159], v[80:87], v[20:23], v216, v215 op_sel_hi:[0,0,0]
	v_mfma_scale_f32_16x16x128_f8f6f4 v[228:231], v[144:151], v[88:95], v[0:3], v216, v215 op_sel_hi:[0,0,0]
	v_mfma_scale_f32_16x16x128_f8f6f4 v[220:223], v[152:159], v[88:95], v[4:7], v216, v215 op_sel_hi:[0,0,0]
	s_setprio 0
	s_barrier
; #define PG8_STAGE(bufoff, gbase, voff) do { const char* sb_ = (gbase); _Pragma("unroll") for (int _i = 0; _i < 2; ++_i) PG8_GLDS(sb_, (voff)[_i], bufoff, _i); } while (0)
; #define PG8_LDA(dst, b, h) do { if constexpr (F8) { _Pragma("unroll") for (int m = 0; m < 4; ++m) dst##8[m] = PG8_RD8(lds + PG8_SA(b, h) + aoff + m * 2048); } else { \
;         _Pragma("unroll") for (int m = 0; m < 4; ++m) _Pragma("unroll") for (int k = 0; k < 2; ++k) dst[m][k] = *(const PG8_LAS bf16x8*)(lds + PG8_SA(b, h) + aoff + m * 2048 + k * 1024); } } while (0)
; #define PG8_LDB(dst, b, h) do { if constexpr (F8) { _Pragma("unroll") for (int n = 0; n < 2; ++n) dst##8[n] = PG8_RD8(lds + PG8_SB(b, h) + boff + n * 2048); } else { \
;         _Pragma("unroll") for (int n = 0; n < 2; ++n) _Pragma("unroll") for (int k = 0; k < 2; ++k) dst[n][k] = *(const PG8_LAS bf16x8*)(lds + PG8_SB(b, h) + boff + n * 2048 + k * 1024); } } while (0)
; #define PG8_WAIT_V(n) asm volatile("s_waitcnt vmcnt(" #n ")" ::: "memory")
; #define PG8_WAIT_L(n) asm volatile("s_waitcnt lgkmcnt(" #n ")" ::: "memory")
; #define PG8_BAR __builtin_amdgcn_s_barrier()
; #define PG8_SCHED __builtin_amdgcn_sched_barrier(0)
;     ...
;             PG8_LDB(B0, 1, 0); PG8_LDB(B1, 1, 1); PG8_SCHED; PG8_LDA(At, 1, 0); PG8_STAGE_A(PG8_SA(0, 1), 1, k2, last);
;             PG8_WAIT_V(8); PG8_WAIT_L(0); PG8_BAR; PG8_MMA(0, 0, At, B0); PG8_MMA(0, 1, At, B1); PG8_BAR; PG8_SCHED;
;             PG8_LDA(At, 1, 1); PG8_STAGE(PG8_SB(1, 0), b3, voffB); PG8_STAGE(PG8_SB(1, 1), b3 + hstep, voffB); PG8_STAGE_A(PG8_SA(1, 0), 0, k3, last);
;             PG8_WAIT_V(8); PG8_WAIT_L(0); PG8_BAR; PG8_MMA(1, 0, At, B0); PG8_MMA(1, 1, At, B1); PG8_BAR; PG8_SCHED;
;         }
	s_nop 3
	ds_read_b128 v[0:3], v217
	ds_read_b128 v[4:7], v217 offset:16
	ds_read_b128 v[12:15], v217 offset:2048
	ds_read_b128 v[16:19], v217 offset:2064
	ds_read_b128 v[128:131], v218
	ds_read_b128 v[132:135], v218 offset:16
	ds_read_b128 v[136:139], v218 offset:2048
	ds_read_b128 v[140:143], v218 offset:2064
	ds_read_b128 v[20:23], v214 offset:32768
	ds_read_b128 v[24:27], v214 offset:32784
	ds_read_b128 v[28:31], v214 offset:34816
	ds_read_b128 v[32:35], v214 offset:34832
	ds_read_b128 v[36:39], v214 offset:36864
	ds_read_b128 v[40:43], v214 offset:36880
	ds_read_b128 v[44:47], v214 offset:38912
	ds_read_b128 v[48:51], v214 offset:38928
	s_add_u32 s78, s30, 0x40000
	s_addc_u32 s79, s31, 0
	s_mov_b32 m0, s58
	s_nop 0
	global_load_lds_dwordx4 v208, s[78:79]
	s_nop 0
	s_mov_b32 m0, s59
	s_nop 0
	global_load_lds_dwordx4 v210, s[78:79]
	s_waitcnt vmcnt(8)
	s_waitcnt lgkmcnt(0)
	s_barrier
	s_setprio 1
	v_mfma_scale_f32_16x16x128_f8f6f4 v[120:123], v[0:7], v[20:27], v[120:123], v216, v215 op_sel_hi:[0,0,0]
	v_mfma_scale_f32_16x16x128_f8f6f4 v[124:127], v[12:19], v[20:27], v[124:127], v216, v215 op_sel_hi:[0,0,0]
	v_mfma_scale_f32_16x16x128_f8f6f4 v[104:107], v[0:7], v[28:35], v[104:107], v216, v215 op_sel_hi:[0,0,0]
	v_mfma_scale_f32_16x16x128_f8f6f4 v[108:111], v[12:19], v[28:35], v[108:111], v216, v215 op_sel_hi:[0,0,0]
	v_mfma_scale_f32_16x16x128_f8f6f4 v[88:91], v[0:7], v[36:43], v[198:201], v216, v215 op_sel_hi:[0,0,0]
	v_mfma_scale_f32_16x16x128_f8f6f4 v[92:95], v[12:19], v[36:43], v[202:205], v216, v215 op_sel_hi:[0,0,0]
	v_mfma_scale_f32_16x16x128_f8f6f4 v[72:75], v[0:7], v[44:51], v[232:235], v216, v215 op_sel_hi:[0,0,0]
	v_mfma_scale_f32_16x16x128_f8f6f4 v[76:79], v[12:19], v[44:51], v[236:239], v216, v215 op_sel_hi:[0,0,0]
	s_setprio 0
	s_setprio 1
	v_mfma_scale_f32_16x16x128_f8f6f4 v[112:115], v[128:135], v[20:27], v[112:115], v216, v215 op_sel_hi:[0,0,0]
	v_mfma_scale_f32_16x16x128_f8f6f4 v[116:119], v[136:143], v[20:27], v[116:119], v216, v215 op_sel_hi:[0,0,0]
	v_mfma_scale_f32_16x16x128_f8f6f4 v[96:99], v[128:135], v[28:35], v[96:99], v216, v215 op_sel_hi:[0,0,0]
	v_mfma_scale_f32_16x16x128_f8f6f4 v[100:103], v[136:143], v[28:35], v[100:103], v216, v215 op_sel_hi:[0,0,0]
	v_mfma_scale_f32_16x16x128_f8f6f4 v[80:83], v[128:135], v[36:43], v[160:163], v216, v215 op_sel_hi:[0,0,0]
	v_mfma_scale_f32_16x16x128_f8f6f4 v[84:87], v[136:143], v[36:43], v[164:167], v216, v215 op_sel_hi:[0,0,0]
	v_mfma_scale_f32_16x16x128_f8f6f4 v[64:67], v[128:135], v[44:51], v[168:171], v216, v215 op_sel_hi:[0,0,0]
	v_mfma_scale_f32_16x16x128_f8f6f4 v[68:71], v[136:143], v[44:51], v[172:175], v216, v215 op_sel_hi:[0,0,0]
	s_setprio 0
	s_barrier
	ds_read_b128 v[32:35], v214 offset:49152
	ds_read_b128 v[36:39], v214 offset:49168
	ds_read_b128 v[144:147], v214 offset:51200
	ds_read_b128 v[148:151], v214 offset:51216
	ds_read_b128 v[152:155], v214 offset:53248
	ds_read_b128 v[156:159], v214 offset:53264
	ds_read_b128 v[160:163], v214 offset:55296
	ds_read_b128 v[164:167], v214 offset:55312
	s_add_u32 s78, s28, 0x80
	s_addc_u32 s79, s29, 0
	s_mov_b32 m0, s63
	s_nop 0
	global_load_lds_dwordx4 v209, s[78:79]
	s_add_u32 s28, s28, 0x40080
	s_mov_b32 m0, s64
	s_nop 0
	global_load_lds_dwordx4 v211, s[78:79]
	s_addc_u32 s29, s29, 0
	s_mov_b32 m0, s67
	s_nop 0
	global_load_lds_dwordx4 v209, s[28:29]
	s_nop 0
	s_mov_b32 m0, s74
	s_nop 0
	global_load_lds_dwordx4 v211, s[28:29]
	s_add_u32 s28, s30, 0x80
	s_addc_u32 s29, s31, 0
	s_mov_b32 m0, s65
	s_nop 0
	global_load_lds_dwordx4 v208, s[28:29]
	s_nop 0
	s_mov_b32 m0, s66
	s_nop 0
	global_load_lds_dwordx4 v210, s[28:29]
	s_waitcnt vmcnt(8)
	s_waitcnt lgkmcnt(0)
	s_barrier
	s_setprio 1
	v_mfma_scale_f32_16x16x128_f8f6f4 v[56:59], v[0:7], v[32:39], v[56:59], v216, v215 op_sel_hi:[0,0,0]
	v_mfma_scale_f32_16x16x128_f8f6f4 v[60:63], v[12:19], v[32:39], v[60:63], v216, v215 op_sel_hi:[0,0,0]
	v_mfma_scale_f32_16x16x128_f8f6f4 v[40:43], v[0:7], v[144:151], v[176:179], v216, v215 op_sel_hi:[0,0,0]
	v_mfma_scale_f32_16x16x128_f8f6f4 v[44:47], v[12:19], v[144:151], v[180:183], v216, v215 op_sel_hi:[0,0,0]
	v_mfma_scale_f32_16x16x128_f8f6f4 v[24:27], v[0:7], v[152:159], v[184:187], v216, v215 op_sel_hi:[0,0,0]
	v_mfma_scale_f32_16x16x128_f8f6f4 v[28:31], v[12:19], v[152:159], v[188:191], v216, v215 op_sel_hi:[0,0,0]
	v_mfma_scale_f32_16x16x128_f8f6f4 v[8:11], v[0:7], v[160:167], v[8:11], v216, v215 op_sel_hi:[0,0,0]
	v_mfma_scale_f32_16x16x128_f8f6f4 v[12:15], v[12:19], v[160:167], v[240:243], v216, v215 op_sel_hi:[0,0,0]
	s_setprio 0
	s_setprio 1
	v_mfma_scale_f32_16x16x128_f8f6f4 v[48:51], v[128:135], v[32:39], v[244:247], v216, v215 op_sel_hi:[0,0,0]
	v_mfma_scale_f32_16x16x128_f8f6f4 v[52:55], v[136:143], v[32:39], v[52:55], v216, v215 op_sel_hi:[0,0,0]
	v_mfma_scale_f32_16x16x128_f8f6f4 v[32:35], v[128:135], v[144:151], v[248:251], v216, v215 op_sel_hi:[0,0,0]
	v_mfma_scale_f32_16x16x128_f8f6f4 v[36:39], v[136:143], v[144:151], v[252:255], v216, v215 op_sel_hi:[0,0,0]
	v_mfma_scale_f32_16x16x128_f8f6f4 v[16:19], v[128:135], v[152:159], v[224:227], v216, v215 op_sel_hi:[0,0,0]
	v_mfma_scale_f32_16x16x128_f8f6f4 v[20:23], v[136:143], v[152:159], v[192:195], v216, v215 op_sel_hi:[0,0,0]
	v_mfma_scale_f32_16x16x128_f8f6f4 v[0:3], v[128:135], v[160:167], v[228:231], v216, v215 op_sel_hi:[0,0,0]
	v_mfma_scale_f32_16x16x128_f8f6f4 v[4:7], v[136:143], v[160:167], v[220:223], v216, v215 op_sel_hi:[0,0,0]
	s_setprio 0
	s_add_i32 s19, s19, 2
	s_add_u32 s26, s26, 0x100
	s_addc_u32 s27, s27, 0
	s_cmp_gt_u32 s19, 13
	s_barrier
	s_cbranch_scc0 .LBB4_306
	s_and_b64 vcc, exec, s[16:17]
	s_cbranch_vccz .LBB4_309
	s_barrier

; #define PG8_STAGE(bufoff, gbase, voff) do { const char* sb_ = (gbase); _Pragma("unroll") for (int _i = 0; _i < 2; ++_i) PG8_GLDS(sb_, (voff)[_i], bufoff, _i); } while (0)
; #define PG8_LDA(dst, b, h) do { if constexpr (F8) { _Pragma("unroll") for (int m = 0; m < 4; ++m) dst##8[m] = PG8_RD8(lds + PG8_SA(b, h) + aoff + m * 2048); } else { \
;         _Pragma("unroll") for (int m = 0; m < 4; ++m) _Pragma("unroll") for (int k = 0; k < 2; ++k) dst[m][k] = *(const PG8_LAS bf16x8*)(lds + PG8_SA(b, h) + aoff + m * 2048 + k * 1024); } } while (0)
; #define PG8_LDB(dst, b, h) do { if constexpr (F8) { _Pragma("unroll") for (int n = 0; n < 2; ++n) dst##8[n] = PG8_RD8(lds + PG8_SB(b, h) + boff + n * 2048); } else { \
;         _Pragma("unroll") for (int n = 0; n < 2; ++n) _Pragma("unroll") for (int k = 0; k < 2; ++k) dst[n][k] = *(const PG8_LAS bf16x8*)(lds + PG8_SB(b, h) + boff + n * 2048 + k * 1024); } } while (0)
; #define PG8_WAIT_V(n) asm volatile("s_waitcnt vmcnt(" #n ")" ::: "memory")
; #define PG8_WAIT_L(n) asm volatile("s_waitcnt lgkmcnt(" #n ")" ::: "memory")
; #define PG8_BAR __builtin_amdgcn_s_barrier()
; #define PG8_SCHED __builtin_amdgcn_sched_barrier(0)
;     ...
;             PG8_LDB(B0, 0, 0); PG8_LDB(B1, 0, 1); PG8_SCHED; PG8_LDA(At, 0, 0); PG8_STAGE_A(PG8_SA(1, 1), 1, k1, false);
;             PG8_WAIT_V(8); PG8_WAIT_L(0); PG8_BAR; PG8_MMA(0, 0, At, B0); PG8_MMA(0, 1, At, B1); PG8_BAR; PG8_SCHED;
;             PG8_LDA(At, 0, 1); PG8_STAGE(PG8_SB(0, 0), b2, voffB); PG8_STAGE(PG8_SB(0, 1), b2 + hstep, voffB); PG8_STAGE_A(PG8_SA(0, 0), 0, k2, last);
;             PG8_WAIT_V(8); PG8_WAIT_L(0); PG8_BAR; PG8_MMA(1, 0, At, B0); PG8_MMA(1, 1, At, B1); PG8_BAR; PG8_SCHED;
.LBB4_1055:
	ds_read_b128 v[152:155], v149
	ds_read_b128 v[156:159], v149 offset:1024
	ds_read_b128 v[160:163], v149 offset:2048
	ds_read_b128 v[164:167], v149 offset:3072
	ds_read_b128 v[168:171], v150
	ds_read_b128 v[172:175], v150 offset:1024
	ds_read_b128 v[176:179], v150 offset:2048
	ds_read_b128 v[180:183], v150 offset:3072
	s_add_u32 s36, s34, 0x100
	s_addc_u32 s37, s35, 0
	s_add_u32 s80, s77, s34
	s_addc_u32 s81, s78, s35
	s_cmp_eq_u32 s79, 28
	s_cselect_b64 s[40:41], -1, 0
	s_and_b64 s[38:39], s[40:41], exec
	s_cselect_b32 s82, 0, s36
	s_cselect_b32 s39, s21, s81
	s_cselect_b32 s38, s23, s80
	v_lshl_add_u64 v[216:217], v[144:145], 0, s[34:35]
	s_add_i32 m0, s29, 0xc000
	ds_read_b128 v[184:187], v151
	ds_read_b128 v[188:191], v151 offset:1024
	ds_read_b128 v[192:195], v151 offset:2048
	ds_read_b128 v[196:199], v151 offset:3072
	ds_read_b128 v[200:203], v151 offset:4096
	ds_read_b128 v[204:207], v151 offset:5120
	ds_read_b128 v[208:211], v151 offset:6144
	ds_read_b128 v[212:215], v151 offset:7168
	global_load_lds_dwordx4 v[216:217], off
	v_lshl_add_u64 v[216:217], v[146:147], 0, s[34:35]
	s_add_i32 m0, s29, 0xe000
	s_nop 0
	global_load_lds_dwordx4 v[216:217], off
	s_waitcnt vmcnt(8)
	s_waitcnt lgkmcnt(0)
	s_barrier
	s_setprio 1
	v_mfma_f32_16x16x32_bf16 v[124:127], v[152:155], v[184:187], v[124:127]
	v_mfma_f32_16x16x32_bf16 v[120:123], v[160:163], v[184:187], v[120:123]
	v_mfma_f32_16x16x32_bf16 v[112:115], v[152:155], v[192:195], v[112:115]
	v_mfma_f32_16x16x32_bf16 v[104:107], v[160:163], v[192:195], v[104:107]
	v_mfma_f32_16x16x32_bf16 v[96:99], v[152:155], v[200:203], v[96:99]
	v_mfma_f32_16x16x32_bf16 v[88:91], v[160:163], v[200:203], v[88:91]
	v_mfma_f32_16x16x32_bf16 v[80:83], v[152:155], v[208:211], v[80:83]
	v_mfma_f32_16x16x32_bf16 v[72:75], v[160:163], v[208:211], v[72:75]
	v_mfma_f32_16x16x32_bf16 v[124:127], v[156:159], v[188:191], v[124:127]
	v_mfma_f32_16x16x32_bf16 v[120:123], v[164:167], v[188:191], v[120:123]
	v_mfma_f32_16x16x32_bf16 v[112:115], v[156:159], v[196:199], v[112:115]
	v_mfma_f32_16x16x32_bf16 v[104:107], v[164:167], v[196:199], v[104:107]
	v_mfma_f32_16x16x32_bf16 v[96:99], v[156:159], v[204:207], v[96:99]
	v_mfma_f32_16x16x32_bf16 v[88:91], v[164:167], v[204:207], v[88:91]
	v_mfma_f32_16x16x32_bf16 v[80:83], v[156:159], v[212:215], v[80:83]
	v_mfma_f32_16x16x32_bf16 v[72:75], v[164:167], v[212:215], v[72:75]
	s_setprio 0
	s_setprio 1
	v_mfma_f32_16x16x32_bf16 v[116:119], v[168:171], v[184:187], v[116:119]
	v_mfma_f32_16x16x32_bf16 v[108:111], v[176:179], v[184:187], v[108:111]
	v_mfma_f32_16x16x32_bf16 v[100:103], v[168:171], v[192:195], v[100:103]
	v_mfma_f32_16x16x32_bf16 v[92:95], v[176:179], v[192:195], v[92:95]
	v_mfma_f32_16x16x32_bf16 v[84:87], v[168:171], v[200:203], v[84:87]
	v_mfma_f32_16x16x32_bf16 v[76:79], v[176:179], v[200:203], v[76:79]
	v_mfma_f32_16x16x32_bf16 v[68:71], v[168:171], v[208:211], v[68:71]
	v_mfma_f32_16x16x32_bf16 v[64:67], v[176:179], v[208:211], v[64:67]
	v_mfma_f32_16x16x32_bf16 v[116:119], v[172:175], v[188:191], v[116:119]
	v_mfma_f32_16x16x32_bf16 v[108:111], v[180:183], v[188:191], v[108:111]
	v_mfma_f32_16x16x32_bf16 v[100:103], v[172:175], v[196:199], v[100:103]
	v_mfma_f32_16x16x32_bf16 v[92:95], v[180:183], v[196:199], v[92:95]
	v_mfma_f32_16x16x32_bf16 v[84:87], v[172:175], v[204:207], v[84:87]
	v_mfma_f32_16x16x32_bf16 v[76:79], v[180:183], v[204:207], v[76:79]
	v_mfma_f32_16x16x32_bf16 v[68:71], v[172:175], v[212:215], v[68:71]
	v_mfma_f32_16x16x32_bf16 v[64:67], v[180:183], v[212:215], v[64:67]
	s_setprio 0
	s_barrier
	s_add_i32 s34, s67, s57
	v_lshl_add_u64 v[216:217], s[38:39], 0, v[130:131]
	s_mov_b32 m0, s34
	ds_read_b128 v[184:187], v151 offset:16384
	ds_read_b128 v[188:191], v151 offset:17408
	ds_read_b128 v[192:195], v151 offset:18432
	ds_read_b128 v[196:199], v151 offset:19456
	ds_read_b128 v[200:203], v151 offset:20480
	ds_read_b128 v[204:207], v151 offset:21504
	ds_read_b128 v[208:211], v151 offset:22528
	ds_read_b128 v[212:215], v151 offset:23552
	global_load_lds_dwordx4 v[216:217], off
	s_add_i32 m0, s34, 0x2000
	s_add_u32 s34, s38, 0x80000
	v_lshl_add_u64 v[218:219], s[38:39], 0, v[134:135]
	s_addc_u32 s35, s39, 0
	s_add_i32 s80, s74, s57
	global_load_lds_dwordx4 v[218:219], off
	v_lshl_add_u64 v[220:221], s[34:35], 0, v[130:131]
	s_mov_b32 m0, s80
	s_nop 0
	global_load_lds_dwordx4 v[220:221], off
	v_lshl_add_u64 v[220:221], s[34:35], 0, v[134:135]
	s_add_i32 m0, s80, 0x2000
	s_and_b64 s[34:35], s[2:3], s[40:41]
	s_and_b64 s[34:35], s[34:35], exec
	s_cselect_b32 s34, s24, s30
	s_cselect_b32 s35, s25, s31
	s_add_u32 s34, s34, s82
	s_addc_u32 s35, s35, 0
	global_load_lds_dwordx4 v[220:221], off
	v_lshl_add_u64 v[220:221], s[34:35], 0, v[128:129]
	s_mov_b32 m0, s29
	v_lshl_add_u64 v[222:223], s[34:35], 0, v[132:133]
	global_load_lds_dwordx4 v[220:221], off
	s_mov_b32 m0, s58
	s_nop 0
	global_load_lds_dwordx4 v[222:223], off
	s_waitcnt vmcnt(8)
	s_waitcnt lgkmcnt(0)
	s_barrier
; #define PG8_LDA(dst, b, h) do { if constexpr (F8) { _Pragma("unroll") for (int m = 0; m < 4; ++m) dst##8[m] = PG8_RD8(lds + PG8_SA(b, h) + aoff + m * 2048); } else { \
;         _Pragma("unroll") for (int m = 0; m < 4; ++m) _Pragma("unroll") for (int k = 0; k < 2; ++k) dst[m][k] = *(const PG8_LAS bf16x8*)(lds + PG8_SA(b, h) + aoff + m * 2048 + k * 1024); } } while (0)
; #define PG8_LDB(dst, b, h) do { if constexpr (F8) { _Pragma("unroll") for (int n = 0; n < 2; ++n) dst##8[n] = PG8_RD8(lds + PG8_SB(b, h) + boff + n * 2048); } else { \
;         _Pragma("unroll") for (int n = 0; n < 2; ++n) _Pragma("unroll") for (int k = 0; k < 2; ++k) dst[n][k] = *(const PG8_LAS bf16x8*)(lds + PG8_SB(b, h) + boff + n * 2048 + k * 1024); } } while (0)
; #define PG8_WAIT_V(n) asm volatile("s_waitcnt vmcnt(" #n ")" ::: "memory")
; #define PG8_WAIT_L(n) asm volatile("s_waitcnt lgkmcnt(" #n ")" ::: "memory")
; #define PG8_BAR __builtin_amdgcn_s_barrier()
; #define PG8_SCHED __builtin_amdgcn_sched_barrier(0)
;     ...
;             PG8_WAIT_V(8); PG8_WAIT_L(0); PG8_BAR; PG8_MMA(1, 0, At, B0); PG8_MMA(1, 1, At, B1); PG8_BAR; PG8_SCHED;
;             PG8_LDB(B0, 1, 0); PG8_LDB(B1, 1, 1); PG8_SCHED; PG8_LDA(At, 1, 0); PG8_STAGE_A(PG8_SA(0, 1), 1, k2, last);
;             PG8_WAIT_V(8); PG8_WAIT_L(0); PG8_BAR; PG8_MMA(0, 0, At, B0); PG8_MMA(0, 1, At, B1); PG8_BAR; PG8_SCHED;
	s_setprio 1
	v_mfma_f32_16x16x32_bf16 v[60:63], v[152:155], v[184:187], v[60:63]
	v_mfma_f32_16x16x32_bf16 v[56:59], v[160:163], v[184:187], v[56:59]
	v_mfma_f32_16x16x32_bf16 v[52:55], v[152:155], v[192:195], v[52:55]
	v_mfma_f32_16x16x32_bf16 v[44:47], v[160:163], v[192:195], v[44:47]
	v_mfma_f32_16x16x32_bf16 v[36:39], v[152:155], v[200:203], v[36:39]
	v_mfma_f32_16x16x32_bf16 v[28:31], v[160:163], v[200:203], v[28:31]
	v_mfma_f32_16x16x32_bf16 v[20:23], v[152:155], v[208:211], v[20:23]
	v_mfma_f32_16x16x32_bf16 v[12:15], v[160:163], v[208:211], v[12:15]
	v_mfma_f32_16x16x32_bf16 v[60:63], v[156:159], v[188:191], v[60:63]
	v_mfma_f32_16x16x32_bf16 v[56:59], v[164:167], v[188:191], v[56:59]
	v_mfma_f32_16x16x32_bf16 v[52:55], v[156:159], v[196:199], v[52:55]
	v_mfma_f32_16x16x32_bf16 v[44:47], v[164:167], v[196:199], v[44:47]
	v_mfma_f32_16x16x32_bf16 v[36:39], v[156:159], v[204:207], v[36:39]
	v_mfma_f32_16x16x32_bf16 v[28:31], v[164:167], v[204:207], v[28:31]
	v_mfma_f32_16x16x32_bf16 v[20:23], v[156:159], v[212:215], v[20:23]
	v_mfma_f32_16x16x32_bf16 v[12:15], v[164:167], v[212:215], v[12:15]
	s_setprio 0
	s_setprio 1
	v_mfma_f32_16x16x32_bf16 v[48:51], v[168:171], v[184:187], v[48:51]
	v_mfma_f32_16x16x32_bf16 v[40:43], v[176:179], v[184:187], v[40:43]
	v_mfma_f32_16x16x32_bf16 v[32:35], v[168:171], v[192:195], v[32:35]
	v_mfma_f32_16x16x32_bf16 v[24:27], v[176:179], v[192:195], v[24:27]
	v_mfma_f32_16x16x32_bf16 v[16:19], v[168:171], v[200:203], v[16:19]
	v_mfma_f32_16x16x32_bf16 v[8:11], v[176:179], v[200:203], v[8:11]
	v_mfma_f32_16x16x32_bf16 v[4:7], v[168:171], v[208:211], v[4:7]
	v_mfma_f32_16x16x32_bf16 v[0:3], v[176:179], v[208:211], v[0:3]
	v_mfma_f32_16x16x32_bf16 v[48:51], v[172:175], v[188:191], v[48:51]
	v_mfma_f32_16x16x32_bf16 v[40:43], v[180:183], v[188:191], v[40:43]
	v_mfma_f32_16x16x32_bf16 v[32:35], v[172:175], v[196:199], v[32:35]
	v_mfma_f32_16x16x32_bf16 v[24:27], v[180:183], v[196:199], v[24:27]
	v_mfma_f32_16x16x32_bf16 v[16:19], v[172:175], v[204:207], v[16:19]
	v_mfma_f32_16x16x32_bf16 v[8:11], v[180:183], v[204:207], v[8:11]
	v_mfma_f32_16x16x32_bf16 v[4:7], v[172:175], v[212:215], v[4:7]
	v_mfma_f32_16x16x32_bf16 v[0:3], v[180:183], v[212:215], v[0:3]
	s_setprio 0
	s_barrier
	s_add_i32 s40, 0, 0x18000
	s_add_i32 s41, 0, 0x1c000
	v_add_u32_e32 v164, s40, v148
	v_add_u32_e32 v180, s41, v148
	ds_read_b128 v[152:155], v164
	ds_read_b128 v[156:159], v164 offset:1024
	ds_read_b128 v[160:163], v164 offset:2048
	ds_read_b128 v[164:167], v164 offset:3072
	ds_read_b128 v[168:171], v180
	ds_read_b128 v[172:175], v180 offset:1024
	ds_read_b128 v[176:179], v180 offset:2048
	ds_read_b128 v[180:183], v180 offset:3072
	s_add_u32 s34, s34, 0x80000
	s_addc_u32 s35, s35, 0
	s_mov_b32 m0, s59
	v_lshl_add_u64 v[224:225], s[34:35], 0, v[128:129]
	ds_read_b128 v[184:187], v151 offset:32768
	ds_read_b128 v[188:191], v151 offset:33792
	ds_read_b128 v[192:195], v151 offset:34816
	ds_read_b128 v[196:199], v151 offset:35840
	ds_read_b128 v[200:203], v151 offset:36864
	ds_read_b128 v[204:207], v151 offset:37888
	ds_read_b128 v[208:211], v151 offset:38912
	ds_read_b128 v[212:215], v151 offset:39936
	global_load_lds_dwordx4 v[224:225], off
	v_lshl_add_u64 v[224:225], s[34:35], 0, v[132:133]
	s_mov_b32 m0, s60
	s_nop 0
	global_load_lds_dwordx4 v[224:225], off
	s_waitcnt vmcnt(8)
	s_waitcnt lgkmcnt(0)
	s_barrier
	s_setprio 1
	v_mfma_f32_16x16x32_bf16 v[124:127], v[152:155], v[184:187], v[124:127]
	v_mfma_f32_16x16x32_bf16 v[120:123], v[160:163], v[184:187], v[120:123]
	v_mfma_f32_16x16x32_bf16 v[112:115], v[152:155], v[192:195], v[112:115]
	v_mfma_f32_16x16x32_bf16 v[104:107], v[160:163], v[192:195], v[104:107]
	v_mfma_f32_16x16x32_bf16 v[96:99], v[152:155], v[200:203], v[96:99]
	v_mfma_f32_16x16x32_bf16 v[88:91], v[160:163], v[200:203], v[88:91]
	v_mfma_f32_16x16x32_bf16 v[80:83], v[152:155], v[208:211], v[80:83]
	v_mfma_f32_16x16x32_bf16 v[72:75], v[160:163], v[208:211], v[72:75]
	v_mfma_f32_16x16x32_bf16 v[124:127], v[156:159], v[188:191], v[124:127]
	v_mfma_f32_16x16x32_bf16 v[120:123], v[164:167], v[188:191], v[120:123]
	v_mfma_f32_16x16x32_bf16 v[112:115], v[156:159], v[196:199], v[112:115]
	v_mfma_f32_16x16x32_bf16 v[104:107], v[164:167], v[196:199], v[104:107]
	v_mfma_f32_16x16x32_bf16 v[96:99], v[156:159], v[204:207], v[96:99]
	v_mfma_f32_16x16x32_bf16 v[88:91], v[164:167], v[204:207], v[88:91]
	v_mfma_f32_16x16x32_bf16 v[80:83], v[156:159], v[212:215], v[80:83]
	v_mfma_f32_16x16x32_bf16 v[72:75], v[164:167], v[212:215], v[72:75]
	s_setprio 0
	s_setprio 1
	v_mfma_f32_16x16x32_bf16 v[116:119], v[168:171], v[184:187], v[116:119]
	v_mfma_f32_16x16x32_bf16 v[108:111], v[176:179], v[184:187], v[108:111]
	v_mfma_f32_16x16x32_bf16 v[100:103], v[168:171], v[192:195], v[100:103]
	v_mfma_f32_16x16x32_bf16 v[92:95], v[176:179], v[192:195], v[92:95]
	v_mfma_f32_16x16x32_bf16 v[84:87], v[168:171], v[200:203], v[84:87]
	v_mfma_f32_16x16x32_bf16 v[76:79], v[176:179], v[200:203], v[76:79]
	v_mfma_f32_16x16x32_bf16 v[68:71], v[168:171], v[208:211], v[68:71]
	v_mfma_f32_16x16x32_bf16 v[64:67], v[176:179], v[208:211], v[64:67]
	v_mfma_f32_16x16x32_bf16 v[116:119], v[172:175], v[188:191], v[116:119]
	v_mfma_f32_16x16x32_bf16 v[108:111], v[180:183], v[188:191], v[108:111]
	v_mfma_f32_16x16x32_bf16 v[100:103], v[172:175], v[196:199], v[100:103]
	v_mfma_f32_16x16x32_bf16 v[92:95], v[180:183], v[196:199], v[92:95]
	v_mfma_f32_16x16x32_bf16 v[84:87], v[172:175], v[204:207], v[84:87]
	v_mfma_f32_16x16x32_bf16 v[76:79], v[180:183], v[204:207], v[76:79]
	v_mfma_f32_16x16x32_bf16 v[68:71], v[172:175], v[212:215], v[68:71]
	v_mfma_f32_16x16x32_bf16 v[64:67], v[180:183], v[212:215], v[64:67]
	s_setprio 0
	s_barrier
; #define PG8_STAGE(bufoff, gbase, voff) do { const char* sb_ = (gbase); _Pragma("unroll") for (int _i = 0; _i < 2; ++_i) PG8_GLDS(sb_, (voff)[_i], bufoff, _i); } while (0)
; #define PG8_LDA(dst, b, h) do { if constexpr (F8) { _Pragma("unroll") for (int m = 0; m < 4; ++m) dst##8[m] = PG8_RD8(lds + PG8_SA(b, h) + aoff + m * 2048); } else { \
;         _Pragma("unroll") for (int m = 0; m < 4; ++m) _Pragma("unroll") for (int k = 0; k < 2; ++k) dst[m][k] = *(const PG8_LAS bf16x8*)(lds + PG8_SA(b, h) + aoff + m * 2048 + k * 1024); } } while (0)
; #define PG8_WAIT_V(n) asm volatile("s_waitcnt vmcnt(" #n ")" ::: "memory")
; #define PG8_WAIT_L(n) asm volatile("s_waitcnt lgkmcnt(" #n ")" ::: "memory")
; #define PG8_BAR __builtin_amdgcn_s_barrier()
; #define PG8_SCHED __builtin_amdgcn_sched_barrier(0)
;     ...
;             PG8_LDA(At, 1, 1); PG8_STAGE(PG8_SB(1, 0), b3, voffB); PG8_STAGE(PG8_SB(1, 1), b3 + hstep, voffB); PG8_STAGE_A(PG8_SA(1, 0), 0, k3, last);
;             PG8_WAIT_V(8); PG8_WAIT_L(0); PG8_BAR; PG8_MMA(1, 0, At, B0); PG8_MMA(1, 1, At, B1); PG8_BAR; PG8_SCHED;
;         }
	s_add_i32 s34, s40, s57
	v_lshl_add_u64 v[216:217], v[216:217], 0, s[8:9]
	s_mov_b32 m0, s34
	ds_read_b128 v[184:187], v151 offset:49152
	ds_read_b128 v[188:191], v151 offset:50176
	ds_read_b128 v[192:195], v151 offset:51200
	ds_read_b128 v[196:199], v151 offset:52224
	ds_read_b128 v[200:203], v151 offset:53248
	ds_read_b128 v[204:207], v151 offset:54272
	ds_read_b128 v[208:211], v151 offset:55296
	ds_read_b128 v[212:215], v151 offset:56320
	global_load_lds_dwordx4 v[216:217], off
	s_add_i32 m0, s34, 0x2000
	s_add_u32 s34, s38, 0x80080
	v_lshl_add_u64 v[216:217], v[218:219], 0, s[8:9]
	s_addc_u32 s35, s39, 0
	s_add_i32 s38, s41, s57
	global_load_lds_dwordx4 v[216:217], off
	v_lshl_add_u64 v[216:217], s[34:35], 0, v[130:131]
	s_mov_b32 m0, s38
	s_nop 0
	global_load_lds_dwordx4 v[216:217], off
	v_lshl_add_u64 v[216:217], s[34:35], 0, v[134:135]
	s_add_i32 m0, s38, 0x2000
	s_nop 0
	global_load_lds_dwordx4 v[216:217], off
	v_lshl_add_u64 v[216:217], v[220:221], 0, s[8:9]
	s_mov_b32 m0, s64
	s_nop 0
	global_load_lds_dwordx4 v[216:217], off
	v_lshl_add_u64 v[216:217], v[222:223], 0, s[8:9]
	s_mov_b32 m0, s65
	s_nop 0
	global_load_lds_dwordx4 v[216:217], off
	s_waitcnt vmcnt(8)
	s_waitcnt lgkmcnt(0)
	s_barrier
	s_setprio 1
	v_mfma_f32_16x16x32_bf16 v[60:63], v[152:155], v[184:187], v[60:63]
	v_mfma_f32_16x16x32_bf16 v[56:59], v[160:163], v[184:187], v[56:59]
	v_mfma_f32_16x16x32_bf16 v[52:55], v[152:155], v[192:195], v[52:55]
	v_mfma_f32_16x16x32_bf16 v[44:47], v[160:163], v[192:195], v[44:47]
	v_mfma_f32_16x16x32_bf16 v[36:39], v[152:155], v[200:203], v[36:39]
	v_mfma_f32_16x16x32_bf16 v[28:31], v[160:163], v[200:203], v[28:31]
	v_mfma_f32_16x16x32_bf16 v[20:23], v[152:155], v[208:211], v[20:23]
	v_mfma_f32_16x16x32_bf16 v[12:15], v[160:163], v[208:211], v[12:15]
	v_mfma_f32_16x16x32_bf16 v[60:63], v[156:159], v[188:191], v[60:63]
	v_mfma_f32_16x16x32_bf16 v[56:59], v[164:167], v[188:191], v[56:59]
	v_mfma_f32_16x16x32_bf16 v[52:55], v[156:159], v[196:199], v[52:55]
	v_mfma_f32_16x16x32_bf16 v[44:47], v[164:167], v[196:199], v[44:47]
	v_mfma_f32_16x16x32_bf16 v[36:39], v[156:159], v[204:207], v[36:39]
	v_mfma_f32_16x16x32_bf16 v[28:31], v[164:167], v[204:207], v[28:31]
	v_mfma_f32_16x16x32_bf16 v[20:23], v[156:159], v[212:215], v[20:23]
	v_mfma_f32_16x16x32_bf16 v[12:15], v[164:167], v[212:215], v[12:15]
	s_setprio 0
	s_setprio 1
	v_mfma_f32_16x16x32_bf16 v[48:51], v[168:171], v[184:187], v[48:51]
	v_mfma_f32_16x16x32_bf16 v[40:43], v[176:179], v[184:187], v[40:43]
	v_mfma_f32_16x16x32_bf16 v[32:35], v[168:171], v[192:195], v[32:35]
	v_mfma_f32_16x16x32_bf16 v[24:27], v[176:179], v[192:195], v[24:27]
	v_mfma_f32_16x16x32_bf16 v[16:19], v[168:171], v[200:203], v[16:19]
	v_mfma_f32_16x16x32_bf16 v[8:11], v[176:179], v[200:203], v[8:11]
	v_mfma_f32_16x16x32_bf16 v[4:7], v[168:171], v[208:211], v[4:7]
	v_mfma_f32_16x16x32_bf16 v[0:3], v[176:179], v[208:211], v[0:3]
	v_mfma_f32_16x16x32_bf16 v[48:51], v[172:175], v[188:191], v[48:51]
	v_mfma_f32_16x16x32_bf16 v[40:43], v[180:183], v[188:191], v[40:43]
	v_mfma_f32_16x16x32_bf16 v[32:35], v[172:175], v[196:199], v[32:35]
	v_mfma_f32_16x16x32_bf16 v[24:27], v[180:183], v[196:199], v[24:27]
	v_mfma_f32_16x16x32_bf16 v[16:19], v[172:175], v[204:207], v[16:19]
	v_mfma_f32_16x16x32_bf16 v[8:11], v[180:183], v[204:207], v[8:11]
	v_mfma_f32_16x16x32_bf16 v[4:7], v[172:175], v[212:215], v[4:7]
	v_mfma_f32_16x16x32_bf16 v[0:3], v[180:183], v[212:215], v[0:3]
	s_setprio 0
	s_add_i32 s79, s79, 2
	s_cmp_gt_u32 s79, 29
	s_mov_b64 s[34:35], s[36:37]
	s_barrier
	s_cbranch_scc0 .LBB4_1055
	s_and_b64 vcc, exec, s[10:11]
	s_cbranch_vccz .LBB4_1058
	s_barrier

; #define PG8_STAGE(bufoff, gbase, voff) do { const char* sb_ = (gbase); _Pragma("unroll") for (int _i = 0; _i < 2; ++_i) PG8_GLDS(sb_, (voff)[_i], bufoff, _i); } while (0)
; #define PG8_LDA(dst, b, h) do { if constexpr (F8) { _Pragma("unroll") for (int m = 0; m < 4; ++m) dst##8[m] = PG8_RD8(lds + PG8_SA(b, h) + aoff + m * 2048); } else { \
;         _Pragma("unroll") for (int m = 0; m < 4; ++m) _Pragma("unroll") for (int k = 0; k < 2; ++k) dst[m][k] = *(const PG8_LAS bf16x8*)(lds + PG8_SA(b, h) + aoff + m * 2048 + k * 1024); } } while (0)
; #define PG8_LDB(dst, b, h) do { if constexpr (F8) { _Pragma("unroll") for (int n = 0; n < 2; ++n) dst##8[n] = PG8_RD8(lds + PG8_SB(b, h) + boff + n * 2048); } else { \
;         _Pragma("unroll") for (int n = 0; n < 2; ++n) _Pragma("unroll") for (int k = 0; k < 2; ++k) dst[n][k] = *(const PG8_LAS bf16x8*)(lds + PG8_SB(b, h) + boff + n * 2048 + k * 1024); } } while (0)
; #define PG8_WAIT_V(n) asm volatile("s_waitcnt vmcnt(" #n ")" ::: "memory")
; #define PG8_WAIT_L(n) asm volatile("s_waitcnt lgkmcnt(" #n ")" ::: "memory")
; #define PG8_BAR __builtin_amdgcn_s_barrier()
; #define PG8_SCHED __builtin_amdgcn_sched_barrier(0)
;     ...
;             PG8_LDB(B0, 0, 0); PG8_LDB(B1, 0, 1); PG8_SCHED; PG8_LDA(At, 0, 0); PG8_STAGE_A(PG8_SA(1, 1), 1, k1, false);
;             PG8_WAIT_V(8); PG8_WAIT_L(0); PG8_BAR; PG8_MMA(0, 0, At, B0); PG8_MMA(0, 1, At, B1); PG8_BAR; PG8_SCHED;
;             PG8_LDA(At, 0, 1); PG8_STAGE(PG8_SB(0, 0), b2, voffB); PG8_STAGE(PG8_SB(0, 1), b2 + hstep, voffB); PG8_STAGE_A(PG8_SA(0, 0), 0, k2, last);
;             PG8_WAIT_V(8); PG8_WAIT_L(0); PG8_BAR; PG8_MMA(1, 0, At, B0); PG8_MMA(1, 1, At, B1); PG8_BAR; PG8_SCHED;
.LBB4_1452:
	ds_read_b128 v[146:149], v138
	ds_read_b128 v[150:153], v138 offset:16
	ds_read_b128 v[154:157], v138 offset:2048
	ds_read_b128 v[158:161], v138 offset:2064
	ds_read_b128 v[162:165], v139
	ds_read_b128 v[166:169], v139 offset:16
	ds_read_b128 v[170:173], v139 offset:2048
	ds_read_b128 v[174:177], v139 offset:2064
	s_add_u32 s28, s20, s24
	s_addc_u32 s29, s21, s25
	s_cmp_eq_u32 s15, 12
	s_cselect_b64 s[30:31], -1, 0
	s_and_b64 s[26:27], s[30:31], exec
	s_cselect_b32 s82, 0, s24
	s_cselect_b32 s27, s17, s29
	s_cselect_b32 s26, s16, s28
	ds_read_b128 v[178:181], v140
	ds_read_b128 v[182:185], v140 offset:16
	ds_read_b128 v[186:189], v140 offset:2048
	ds_read_b128 v[190:193], v140 offset:2064
	ds_read_b128 v[194:197], v140 offset:4096
	ds_read_b128 v[198:201], v140 offset:4112
	ds_read_b128 v[202:205], v140 offset:6144
	ds_read_b128 v[206:209], v140 offset:6160
	ds_read2st64_b32 v[128:129], v132 offset0:16 offset1:24
	s_add_u32 s28, s6, s24
	s_addc_u32 s29, s7, s25
	s_add_u32 s28, s28, 0xffffff80
	s_addc_u32 s29, s29, -1
	s_waitcnt lgkmcnt(0)
	s_mov_b32 m0, s66
	s_nop 0
	global_load_lds_dwordx4 v128, s[28:29]
	s_nop 0
	s_mov_b32 m0, s67
	s_nop 0
	global_load_lds_dwordx4 v129, s[28:29]
	s_waitcnt vmcnt(8)
	s_waitcnt lgkmcnt(0)
	s_barrier
	s_setprio 1
	v_mfma_scale_f32_16x16x128_f8f6f4 v[124:127], v[146:153], v[178:185], v[124:127], v142, v141 op_sel_hi:[0,0,0]
	v_mfma_scale_f32_16x16x128_f8f6f4 v[120:123], v[154:161], v[178:185], v[120:123], v142, v141 op_sel_hi:[0,0,0]
	v_mfma_scale_f32_16x16x128_f8f6f4 v[108:111], v[146:153], v[186:193], v[108:111], v142, v141 op_sel_hi:[0,0,0]
	v_mfma_scale_f32_16x16x128_f8f6f4 v[104:107], v[154:161], v[186:193], v[104:107], v142, v141 op_sel_hi:[0,0,0]
	v_mfma_scale_f32_16x16x128_f8f6f4 v[210:213], v[146:153], v[194:201], v[92:95], v142, v141 op_sel_hi:[0,0,0]
	v_mfma_scale_f32_16x16x128_f8f6f4 v[214:217], v[154:161], v[194:201], v[88:91], v142, v141 op_sel_hi:[0,0,0]
	v_mfma_scale_f32_16x16x128_f8f6f4 v[218:221], v[146:153], v[202:209], v[76:79], v142, v141 op_sel_hi:[0,0,0]
	v_mfma_scale_f32_16x16x128_f8f6f4 v[222:225], v[154:161], v[202:209], v[72:75], v142, v141 op_sel_hi:[0,0,0]
	s_setprio 0
	s_setprio 1
	v_mfma_scale_f32_16x16x128_f8f6f4 v[116:119], v[162:169], v[178:185], v[116:119], v142, v141 op_sel_hi:[0,0,0]
	v_mfma_scale_f32_16x16x128_f8f6f4 v[112:115], v[170:177], v[178:185], v[112:115], v142, v141 op_sel_hi:[0,0,0]
	v_mfma_scale_f32_16x16x128_f8f6f4 v[100:103], v[162:169], v[186:193], v[100:103], v142, v141 op_sel_hi:[0,0,0]
	v_mfma_scale_f32_16x16x128_f8f6f4 v[96:99], v[170:177], v[186:193], v[96:99], v142, v141 op_sel_hi:[0,0,0]
	v_mfma_scale_f32_16x16x128_f8f6f4 v[178:181], v[162:169], v[194:201], v[84:87], v142, v141 op_sel_hi:[0,0,0]
	v_mfma_scale_f32_16x16x128_f8f6f4 v[182:185], v[170:177], v[194:201], v[80:83], v142, v141 op_sel_hi:[0,0,0]
	v_mfma_scale_f32_16x16x128_f8f6f4 v[186:189], v[162:169], v[202:209], v[68:71], v142, v141 op_sel_hi:[0,0,0]
	v_mfma_scale_f32_16x16x128_f8f6f4 v[190:193], v[170:177], v[202:209], v[64:67], v142, v141 op_sel_hi:[0,0,0]
	s_setprio 0
	s_barrier
	s_nop 4
	ds_read_b128 v[64:67], v140 offset:16384
	ds_read_b128 v[68:71], v140 offset:16400
	ds_read_b128 v[72:75], v140 offset:18432
	ds_read_b128 v[76:79], v140 offset:18448
	ds_read_b128 v[80:83], v140 offset:20480
	ds_read_b128 v[84:87], v140 offset:20496
	ds_read_b128 v[88:91], v140 offset:22528
	ds_read_b128 v[92:95], v140 offset:22544
	s_mov_b32 m0, s19
	s_nop 0
	global_load_lds_dwordx4 v135, s[26:27]
	s_add_u32 s28, s26, 0x40000
	s_mov_b32 m0, s42
	s_nop 0
	global_load_lds_dwordx4 v136, s[26:27]
	s_addc_u32 s29, s27, 0
	s_mov_b32 m0, s43
	s_nop 0
	global_load_lds_dwordx4 v135, s[28:29]
	s_nop 0
	s_mov_b32 m0, s54
	s_nop 0
	global_load_lds_dwordx4 v136, s[28:29]
	s_add_u32 s28, s6, s82
	s_addc_u32 s29, s7, 0
	s_and_b64 s[30:31], s[22:23], s[30:31]
	s_and_b64 s[30:31], s[30:31], exec
	s_cselect_b32 s30, s78, s80
	s_lshl_b32 s30, s30, 13
	s_and_b32 s30, s30, 0x2000
	v_add_u32_e32 v133, s30, v137
	ds_read2st64_b32 v[128:129], v133 offset1:8
	s_waitcnt lgkmcnt(0)
	s_mov_b32 m0, s39
	s_nop 0
	global_load_lds_dwordx4 v128, s[28:29]
	s_nop 0
	s_mov_b32 m0, s55
	s_nop 0
	global_load_lds_dwordx4 v129, s[28:29]
	s_waitcnt vmcnt(8)
	s_waitcnt lgkmcnt(0)
	s_barrier
	s_setprio 1
	v_mfma_scale_f32_16x16x128_f8f6f4 v[60:63], v[146:153], v[64:71], v[60:63], v142, v141 op_sel_hi:[0,0,0]
	v_mfma_scale_f32_16x16x128_f8f6f4 v[56:59], v[154:161], v[64:71], v[56:59], v142, v141 op_sel_hi:[0,0,0]
	v_mfma_scale_f32_16x16x128_f8f6f4 v[194:197], v[146:153], v[72:79], v[44:47], v142, v141 op_sel_hi:[0,0,0]
	v_mfma_scale_f32_16x16x128_f8f6f4 v[198:201], v[154:161], v[72:79], v[40:43], v142, v141 op_sel_hi:[0,0,0]
	v_mfma_scale_f32_16x16x128_f8f6f4 v[202:205], v[146:153], v[80:87], v[28:31], v142, v141 op_sel_hi:[0,0,0]
	v_mfma_scale_f32_16x16x128_f8f6f4 v[206:209], v[154:161], v[80:87], v[24:27], v142, v141 op_sel_hi:[0,0,0]
	v_mfma_scale_f32_16x16x128_f8f6f4 v[226:229], v[146:153], v[88:95], v[12:15], v142, v141 op_sel_hi:[0,0,0]
	v_mfma_scale_f32_16x16x128_f8f6f4 v[230:233], v[154:161], v[88:95], v[8:11], v142, v141 op_sel_hi:[0,0,0]
	s_setprio 0
	s_setprio 1
	v_mfma_scale_f32_16x16x128_f8f6f4 v[52:55], v[162:169], v[64:71], v[52:55], v142, v141 op_sel_hi:[0,0,0]
	v_mfma_scale_f32_16x16x128_f8f6f4 v[48:51], v[170:177], v[64:71], v[48:51], v142, v141 op_sel_hi:[0,0,0]
	v_mfma_scale_f32_16x16x128_f8f6f4 v[234:237], v[162:169], v[72:79], v[36:39], v142, v141 op_sel_hi:[0,0,0]
	v_mfma_scale_f32_16x16x128_f8f6f4 v[238:241], v[170:177], v[72:79], v[32:35], v142, v141 op_sel_hi:[0,0,0]
	v_mfma_scale_f32_16x16x128_f8f6f4 v[242:245], v[162:169], v[80:87], v[20:23], v142, v141 op_sel_hi:[0,0,0]
	v_mfma_scale_f32_16x16x128_f8f6f4 v[246:249], v[170:177], v[80:87], v[16:19], v142, v141 op_sel_hi:[0,0,0]
	v_mfma_scale_f32_16x16x128_f8f6f4 v[250:253], v[162:169], v[88:95], v[4:7], v142, v141 op_sel_hi:[0,0,0]
	v_mfma_scale_f32_16x16x128_f8f6f4 v[128:131], v[170:177], v[88:95], v[0:3], v142, v141 op_sel_hi:[0,0,0]
	s_setprio 0
	s_barrier
; #define PG8_STAGE(bufoff, gbase, voff) do { const char* sb_ = (gbase); _Pragma("unroll") for (int _i = 0; _i < 2; ++_i) PG8_GLDS(sb_, (voff)[_i], bufoff, _i); } while (0)
; #define PG8_LDA(dst, b, h) do { if constexpr (F8) { _Pragma("unroll") for (int m = 0; m < 4; ++m) dst##8[m] = PG8_RD8(lds + PG8_SA(b, h) + aoff + m * 2048); } else { \
;         _Pragma("unroll") for (int m = 0; m < 4; ++m) _Pragma("unroll") for (int k = 0; k < 2; ++k) dst[m][k] = *(const PG8_LAS bf16x8*)(lds + PG8_SA(b, h) + aoff + m * 2048 + k * 1024); } } while (0)
; #define PG8_LDB(dst, b, h) do { if constexpr (F8) { _Pragma("unroll") for (int n = 0; n < 2; ++n) dst##8[n] = PG8_RD8(lds + PG8_SB(b, h) + boff + n * 2048); } else { \
;         _Pragma("unroll") for (int n = 0; n < 2; ++n) _Pragma("unroll") for (int k = 0; k < 2; ++k) dst[n][k] = *(const PG8_LAS bf16x8*)(lds + PG8_SB(b, h) + boff + n * 2048 + k * 1024); } } while (0)
; #define PG8_WAIT_V(n) asm volatile("s_waitcnt vmcnt(" #n ")" ::: "memory")
; #define PG8_WAIT_L(n) asm volatile("s_waitcnt lgkmcnt(" #n ")" ::: "memory")
; #define PG8_BAR __builtin_amdgcn_s_barrier()
; #define PG8_SCHED __builtin_amdgcn_sched_barrier(0)
;     ...
;             PG8_LDB(B0, 1, 0); PG8_LDB(B1, 1, 1); PG8_SCHED; PG8_LDA(At, 1, 0); PG8_STAGE_A(PG8_SA(0, 1), 1, k2, last);
;             PG8_WAIT_V(8); PG8_WAIT_L(0); PG8_BAR; PG8_MMA(0, 0, At, B0); PG8_MMA(0, 1, At, B1); PG8_BAR; PG8_SCHED;
;             PG8_LDA(At, 1, 1); PG8_STAGE(PG8_SB(1, 0), b3, voffB); PG8_STAGE(PG8_SB(1, 1), b3 + hstep, voffB); PG8_STAGE_A(PG8_SA(1, 0), 0, k3, last);
;             PG8_WAIT_V(8); PG8_WAIT_L(0); PG8_BAR; PG8_MMA(1, 0, At, B0); PG8_MMA(1, 1, At, B1); PG8_BAR; PG8_SCHED;
;         }
	s_nop 4
	ds_read_b128 v[0:3], v143
	ds_read_b128 v[4:7], v143 offset:16
	ds_read_b128 v[16:19], v143 offset:2048
	ds_read_b128 v[20:23], v143 offset:2064
	ds_read_b128 v[146:149], v144
	ds_read_b128 v[150:153], v144 offset:16
	ds_read_b128 v[154:157], v144 offset:2048
	ds_read_b128 v[158:161], v144 offset:2064
	ds_read_b128 v[8:11], v140 offset:32768
	ds_read_b128 v[12:15], v140 offset:32784
	ds_read_b128 v[24:27], v140 offset:34816
	ds_read_b128 v[28:31], v140 offset:34832
	ds_read2st64_b32 v[64:65], v133 offset0:16 offset1:24
	ds_read_b128 v[32:35], v140 offset:36864
	ds_read_b128 v[36:39], v140 offset:36880
	ds_read_b128 v[40:43], v140 offset:38912
	ds_read_b128 v[44:47], v140 offset:38928
	s_waitcnt lgkmcnt(4)
	s_mov_b32 m0, s56
	s_nop 0
	global_load_lds_dwordx4 v64, s[28:29]
	s_nop 0
	s_mov_b32 m0, s57
	s_nop 0
	global_load_lds_dwordx4 v65, s[28:29]
	s_waitcnt vmcnt(8)
	s_waitcnt lgkmcnt(0)
	s_barrier
	s_setprio 1
	v_mfma_scale_f32_16x16x128_f8f6f4 v[124:127], v[0:7], v[8:15], v[124:127], v142, v141 op_sel_hi:[0,0,0]
	v_mfma_scale_f32_16x16x128_f8f6f4 v[120:123], v[16:23], v[8:15], v[120:123], v142, v141 op_sel_hi:[0,0,0]
	v_mfma_scale_f32_16x16x128_f8f6f4 v[108:111], v[0:7], v[24:31], v[108:111], v142, v141 op_sel_hi:[0,0,0]
	v_mfma_scale_f32_16x16x128_f8f6f4 v[104:107], v[16:23], v[24:31], v[104:107], v142, v141 op_sel_hi:[0,0,0]
	v_mfma_scale_f32_16x16x128_f8f6f4 v[92:95], v[0:7], v[32:39], v[210:213], v142, v141 op_sel_hi:[0,0,0]
	v_mfma_scale_f32_16x16x128_f8f6f4 v[88:91], v[16:23], v[32:39], v[214:217], v142, v141 op_sel_hi:[0,0,0]
	v_mfma_scale_f32_16x16x128_f8f6f4 v[76:79], v[0:7], v[40:47], v[218:221], v142, v141 op_sel_hi:[0,0,0]
	v_mfma_scale_f32_16x16x128_f8f6f4 v[72:75], v[16:23], v[40:47], v[222:225], v142, v141 op_sel_hi:[0,0,0]
	s_setprio 0
	s_setprio 1
	v_mfma_scale_f32_16x16x128_f8f6f4 v[116:119], v[146:153], v[8:15], v[116:119], v142, v141 op_sel_hi:[0,0,0]
	v_mfma_scale_f32_16x16x128_f8f6f4 v[112:115], v[154:161], v[8:15], v[112:115], v142, v141 op_sel_hi:[0,0,0]
	v_mfma_scale_f32_16x16x128_f8f6f4 v[100:103], v[146:153], v[24:31], v[100:103], v142, v141 op_sel_hi:[0,0,0]
	v_mfma_scale_f32_16x16x128_f8f6f4 v[96:99], v[154:161], v[24:31], v[96:99], v142, v141 op_sel_hi:[0,0,0]
	v_mfma_scale_f32_16x16x128_f8f6f4 v[84:87], v[146:153], v[32:39], v[178:181], v142, v141 op_sel_hi:[0,0,0]
	v_mfma_scale_f32_16x16x128_f8f6f4 v[80:83], v[154:161], v[32:39], v[182:185], v142, v141 op_sel_hi:[0,0,0]
	v_mfma_scale_f32_16x16x128_f8f6f4 v[68:71], v[146:153], v[40:47], v[186:189], v142, v141 op_sel_hi:[0,0,0]
	v_mfma_scale_f32_16x16x128_f8f6f4 v[64:67], v[154:161], v[40:47], v[190:193], v142, v141 op_sel_hi:[0,0,0]
	s_setprio 0
	s_barrier
	ds_read_b128 v[32:35], v140 offset:49152
	ds_read_b128 v[36:39], v140 offset:49168
	ds_read_b128 v[162:165], v140 offset:51200
	ds_read_b128 v[166:169], v140 offset:51216
	ds_read_b128 v[170:173], v140 offset:53248
	ds_read_b128 v[174:177], v140 offset:53264
	ds_read_b128 v[178:181], v140 offset:55296
	ds_read_b128 v[182:185], v140 offset:55312
	s_add_u32 s30, s26, 0x80
	s_addc_u32 s31, s27, 0
	s_mov_b32 m0, s60
	s_nop 0
	global_load_lds_dwordx4 v135, s[30:31]
	s_add_u32 s26, s26, 0x40080
	s_mov_b32 m0, s61
	s_nop 0
	global_load_lds_dwordx4 v136, s[30:31]
	s_addc_u32 s27, s27, 0
	s_mov_b32 m0, s64
	s_nop 0
	global_load_lds_dwordx4 v135, s[26:27]
	s_nop 0
	s_mov_b32 m0, s65
	s_nop 0
	global_load_lds_dwordx4 v136, s[26:27]
	s_add_u32 s26, s28, 0x80
	ds_read2st64_b32 v[8:9], v133 offset1:8
	s_addc_u32 s27, s29, 0
	s_waitcnt lgkmcnt(0)
	s_mov_b32 m0, s62
	s_nop 0
	global_load_lds_dwordx4 v8, s[26:27]
	s_nop 0
	s_mov_b32 m0, s63
	s_nop 0
	global_load_lds_dwordx4 v9, s[26:27]
	s_waitcnt vmcnt(8)
	s_waitcnt lgkmcnt(0)
	s_barrier
	s_setprio 1
	v_mfma_scale_f32_16x16x128_f8f6f4 v[60:63], v[0:7], v[32:39], v[60:63], v142, v141 op_sel_hi:[0,0,0]
	v_mfma_scale_f32_16x16x128_f8f6f4 v[56:59], v[16:23], v[32:39], v[56:59], v142, v141 op_sel_hi:[0,0,0]
	v_mfma_scale_f32_16x16x128_f8f6f4 v[44:47], v[0:7], v[162:169], v[194:197], v142, v141 op_sel_hi:[0,0,0]
	v_mfma_scale_f32_16x16x128_f8f6f4 v[40:43], v[16:23], v[162:169], v[198:201], v142, v141 op_sel_hi:[0,0,0]
	v_mfma_scale_f32_16x16x128_f8f6f4 v[28:31], v[0:7], v[170:177], v[202:205], v142, v141 op_sel_hi:[0,0,0]
	v_mfma_scale_f32_16x16x128_f8f6f4 v[24:27], v[16:23], v[170:177], v[206:209], v142, v141 op_sel_hi:[0,0,0]
	v_mfma_scale_f32_16x16x128_f8f6f4 v[12:15], v[0:7], v[178:185], v[226:229], v142, v141 op_sel_hi:[0,0,0]
	v_mfma_scale_f32_16x16x128_f8f6f4 v[8:11], v[16:23], v[178:185], v[230:233], v142, v141 op_sel_hi:[0,0,0]
	s_setprio 0
	s_setprio 1
	v_mfma_scale_f32_16x16x128_f8f6f4 v[52:55], v[146:153], v[32:39], v[52:55], v142, v141 op_sel_hi:[0,0,0]
	v_mfma_scale_f32_16x16x128_f8f6f4 v[48:51], v[154:161], v[32:39], v[48:51], v142, v141 op_sel_hi:[0,0,0]
	v_mfma_scale_f32_16x16x128_f8f6f4 v[36:39], v[146:153], v[162:169], v[234:237], v142, v141 op_sel_hi:[0,0,0]
	v_mfma_scale_f32_16x16x128_f8f6f4 v[32:35], v[154:161], v[162:169], v[238:241], v142, v141 op_sel_hi:[0,0,0]
	v_mfma_scale_f32_16x16x128_f8f6f4 v[20:23], v[146:153], v[170:177], v[242:245], v142, v141 op_sel_hi:[0,0,0]
	v_mfma_scale_f32_16x16x128_f8f6f4 v[16:19], v[154:161], v[170:177], v[246:249], v142, v141 op_sel_hi:[0,0,0]
	v_mfma_scale_f32_16x16x128_f8f6f4 v[4:7], v[146:153], v[178:185], v[250:253], v142, v141 op_sel_hi:[0,0,0]
	v_mfma_scale_f32_16x16x128_f8f6f4 v[0:3], v[154:161], v[178:185], v[128:131], v142, v141 op_sel_hi:[0,0,0]
	s_setprio 0
	s_add_i32 s15, s15, 2
	s_add_u32 s24, s24, 0x100
	s_addc_u32 s25, s25, 0
	s_cmp_gt_u32 s15, 13
	s_barrier
	s_cbranch_scc0 .LBB4_1452
	s_and_b64 vcc, exec, s[12:13]
	s_cbranch_vccz .LBB4_1455
	s_barrier
; DI unsigned pk4_f8(float a, float b, float c, float d) {
;     a = __builtin_amdgcn_fmed3f(a, -448.f, 448.f); b = __builtin_amdgcn_fmed3f(b, -448.f, 448.f); c = __builtin_amdgcn_fmed3f(c, -448.f, 448.f); d = __builtin_amdgcn_fmed3f(d, -448.f, 448.f);
;     int w = __builtin_amdgcn_cvt_pk_fp8_f32(a, b, 0, false); w = __builtin_amdgcn_cvt_pk_fp8_f32(c, d, w, true); return (unsigned)w; }
; DI float silu_f(float v) { return v * __builtin_amdgcn_rcpf(1.f + __builtin_amdgcn_exp2f(-1.4426950408889634f * v)); }
.LBB4_1455:
	s_mov_b32 s94, 0x3e800000
	s_lshl_b32 s15, s81, 8
	v_mul_f32_e32 v129, 0xbfb8aa3b, v124
	s_add_i32 s15, s15, s58
	v_exp_f32_e32 v129, v129
	v_mul_f32_e32 v131, 0xbfb8aa3b, v125
	v_mbcnt_lo_u32_b32 v128, -1, 0
	v_mbcnt_hi_u32_b32 v128, -1, v128
	v_exp_f32_e32 v131, v131
	v_and_or_b32 v130, v128, 15, s15
	s_lshl_b32 s15, s18, 7
	s_and_b32 s15, s15, 0x780
	v_ashrrev_i32_e32 v128, 1, v128
	s_or_b32 s15, s15, s59
	v_and_b32_e32 v128, -8, v128
	v_add_u32_e32 v132, s15, v128
	v_fma_f32 v128, v129, s94, s94
	v_rcp_f32_e32 v128, v128
	v_fma_f32 v129, v131, s94, s94
	v_rcp_f32_e32 v129, v129
	v_ashrrev_i32_e32 v131, 31, v130
	v_mul_f32_e32 v124, v124, v128
	v_mul_f32_e32 v116, v124, v116
	v_mul_f32_e32 v124, v125, v129
	v_mul_f32_e32 v125, 0xbfb8aa3b, v126
	v_exp_f32_e32 v125, v125
	v_mul_f32_e32 v128, 0xbfb8aa3b, v127
	v_exp_f32_e32 v128, v128
	v_mul_f32_e32 v117, v124, v117
	v_fma_f32 v124, v125, s94, s94
	v_rcp_f32_e32 v124, v124
	v_fma_f32 v125, v128, s94, s94
	v_mul_f32_e32 v128, 0xbfb8aa3b, v120
	v_rcp_f32_e32 v125, v125
	v_exp_f32_e32 v128, v128
	v_mul_f32_e32 v124, v126, v124
	v_mul_f32_e32 v118, v124, v118
	v_mul_f32_e32 v124, v127, v125
	v_fma_f32 v125, v128, s94, s94
	v_rcp_f32_e32 v125, v125
	v_mul_f32_e32 v126, 0xbfb8aa3b, v121
	v_exp_f32_e32 v126, v126
	v_mul_f32_e32 v119, v124, v119
	v_mul_f32_e32 v120, v120, v125
	v_mul_f32_e32 v112, v120, v112
	v_fma_f32 v120, v126, s94, s94
	v_mul_f32_e32 v124, 0xbfb8aa3b, v122
	v_rcp_f32_e32 v120, v120
	v_exp_f32_e32 v124, v124
	v_mul_f32_e32 v125, 0xbfb8aa3b, v123
	v_exp_f32_e32 v125, v125
	v_mul_f32_e32 v120, v121, v120
	v_fma_f32 v121, v124, s94, s94
	v_rcp_f32_e32 v121, v121
	v_fma_f32 v124, v125, s94, s94
	v_rcp_f32_e32 v124, v124
	v_mul_f32_e32 v113, v120, v113
	v_mul_f32_e32 v120, v122, v121
	v_mul_f32_e32 v120, v120, v114
	v_mul_f32_e32 v114, v123, v124
	v_mul_f32_e32 v121, v114, v115
	v_mov_b32_e32 v115, v117
	v_med3_f32 v117, v116, s74, v145
	v_med3_f32 v115, v115, s74, v145
	v_cvt_pk_fp8_f32 v114, v117, v115
	v_med3_f32 v116, v118, s74, v145
	v_med3_f32 v115, v119, s74, v145
	v_cvt_pk_fp8_f32 v114, v116, v115 op_sel:[0,0,1]
	v_med3_f32 v112, v112, s74, v145
	v_med3_f32 v113, v113, s74, v145
	v_cvt_pk_fp8_f32 v115, v112, v113
	v_med3_f32 v113, v120, s74, v145
	v_mul_f32_e32 v116, 0xbfb8aa3b, v108
	v_exp_f32_e32 v116, v116
	v_mul_f32_e32 v117, 0xbfb8aa3b, v109
	v_exp_f32_e32 v117, v117
	v_fma_f32 v116, v116, s94, s94
	v_rcp_f32_e32 v116, v116
	v_fma_f32 v117, v117, s94, s94
	v_med3_f32 v112, v121, s74, v145
	v_rcp_f32_e32 v117, v117
	v_cvt_pk_fp8_f32 v115, v113, v112 op_sel:[0,0,1]
	v_lshlrev_b64 v[112:113], 11, v[130:131]
	v_ashrrev_i32_e32 v133, 31, v132
	v_lshl_add_u64 v[112:113], s[10:11], 0, v[112:113]
	v_mul_f32_e32 v108, v108, v116
	v_lshl_add_u64 v[112:113], v[112:113], 0, v[132:133]
	v_mul_f32_e32 v100, v108, v100
	v_mul_f32_e32 v108, v109, v117
	v_mul_f32_e32 v109, 0xbfb8aa3b, v110
	global_store_dwordx2 v[112:113], v[114:115], off
	v_exp_f32_e32 v109, v109
	v_mul_f32_e32 v114, 0xbfb8aa3b, v111
	v_exp_f32_e32 v114, v114
	v_mul_f32_e32 v101, v108, v101
	v_fma_f32 v108, v109, s94, s94
	v_rcp_f32_e32 v108, v108
	v_fma_f32 v109, v114, s94, s94
	v_mul_f32_e32 v114, 0xbfb8aa3b, v104
	v_rcp_f32_e32 v109, v109
	v_exp_f32_e32 v114, v114
	v_mul_f32_e32 v108, v110, v108
	v_mul_f32_e32 v102, v108, v102
	v_mul_f32_e32 v108, v111, v109
	v_fma_f32 v109, v114, s94, s94
	v_rcp_f32_e32 v109, v109
	v_mul_f32_e32 v110, 0xbfb8aa3b, v105
	v_exp_f32_e32 v110, v110
	v_mul_f32_e32 v103, v108, v103
	v_mul_f32_e32 v104, v104, v109
	v_mul_f32_e32 v104, v104, v96
	v_fma_f32 v96, v110, s94, s94
	v_mul_f32_e32 v108, 0xbfb8aa3b, v106
	v_rcp_f32_e32 v96, v96
	v_exp_f32_e32 v108, v108
	v_mul_f32_e32 v109, 0xbfb8aa3b, v107
	v_exp_f32_e32 v109, v109
	v_mul_f32_e32 v96, v105, v96
	v_fma_f32 v105, v108, s94, s94
	v_rcp_f32_e32 v105, v105
	v_fma_f32 v108, v109, s94, s94
	v_rcp_f32_e32 v108, v108
	v_mul_f32_e32 v97, v96, v97
	v_mul_f32_e32 v96, v106, v105
	v_mul_f32_e32 v98, v96, v98
	v_mul_f32_e32 v96, v107, v108
	v_mul_f32_e32 v99, v96, v99
	v_mov_b32_e32 v96, v100
	v_mov_b32_e32 v100, v101
	v_mov_b32_e32 v101, v102
	v_med3_f32 v102, v96, s74, v145
	v_med3_f32 v100, v100, s74, v145
	v_cvt_pk_fp8_f32 v96, v102, v100
	v_med3_f32 v101, v101, s74, v145
	v_med3_f32 v100, v103, s74, v145
	v_cvt_pk_fp8_f32 v96, v101, v100 op_sel:[0,0,1]
	v_med3_f32 v100, v104, s74, v145
	v_med3_f32 v101, v97, s74, v145
	v_cvt_pk_fp8_f32 v97, v100, v101
	v_mul_f32_e32 v100, 0xbfb8aa3b, v92
	v_exp_f32_e32 v100, v100
	v_mul_f32_e32 v101, 0xbfb8aa3b, v93
	v_exp_f32_e32 v101, v101
	v_fma_f32 v100, v100, s94, s94
	v_med3_f32 v98, v98, s74, v145
	v_med3_f32 v99, v99, s74, v145
	v_rcp_f32_e32 v100, v100
	v_fma_f32 v101, v101, s94, s94
	v_cvt_pk_fp8_f32 v97, v98, v99 op_sel:[0,0,1]
	v_or_b32_e32 v98, 16, v130
	v_rcp_f32_e32 v101, v101
	v_ashrrev_i32_e32 v99, 31, v98
	v_lshlrev_b64 v[98:99], 11, v[98:99]
	v_lshl_add_u64 v[98:99], s[10:11], 0, v[98:99]
	v_mul_f32_e32 v92, v92, v100
	v_lshl_add_u64 v[98:99], v[98:99], 0, v[132:133]
	v_mul_f32_e32 v84, v92, v84
	v_mul_f32_e32 v92, v93, v101
	v_mul_f32_e32 v93, 0xbfb8aa3b, v94
	global_store_dwordx2 v[98:99], v[96:97], off
	v_exp_f32_e32 v93, v93
	v_mul_f32_e32 v96, 0xbfb8aa3b, v95
	v_exp_f32_e32 v96, v96
	v_mul_f32_e32 v85, v92, v85
	v_fma_f32 v92, v93, s94, s94
	v_rcp_f32_e32 v92, v92
	v_fma_f32 v93, v96, s94, s94
	v_mul_f32_e32 v96, 0xbfb8aa3b, v88
	v_rcp_f32_e32 v93, v93
	v_exp_f32_e32 v96, v96
	v_mul_f32_e32 v92, v94, v92
	v_mul_f32_e32 v86, v92, v86
	v_mul_f32_e32 v92, v95, v93
	v_fma_f32 v93, v96, s94, s94
	v_rcp_f32_e32 v93, v93
	v_mul_f32_e32 v94, 0xbfb8aa3b, v89
	v_exp_f32_e32 v94, v94
; DI unsigned pk4_f8(float a, float b, float c, float d) {
;     a = __builtin_amdgcn_fmed3f(a, -448.f, 448.f); b = __builtin_amdgcn_fmed3f(b, -448.f, 448.f); c = __builtin_amdgcn_fmed3f(c, -448.f, 448.f); d = __builtin_amdgcn_fmed3f(d, -448.f, 448.f);
;     int w = __builtin_amdgcn_cvt_pk_fp8_f32(a, b, 0, false); w = __builtin_amdgcn_cvt_pk_fp8_f32(c, d, w, true); return (unsigned)w; }
; DI float silu_f(float v) { return v * __builtin_amdgcn_rcpf(1.f + __builtin_amdgcn_exp2f(-1.4426950408889634f * v)); }
	v_mul_f32_e32 v87, v92, v87
	v_mul_f32_e32 v88, v88, v93
	v_mul_f32_e32 v88, v88, v80
	v_fma_f32 v80, v94, s94, s94
	v_mul_f32_e32 v92, 0xbfb8aa3b, v90
	v_rcp_f32_e32 v80, v80
	v_exp_f32_e32 v92, v92
	v_mul_f32_e32 v93, 0xbfb8aa3b, v91
	v_exp_f32_e32 v93, v93
	v_mul_f32_e32 v80, v89, v80
	v_fma_f32 v89, v92, s94, s94
	v_rcp_f32_e32 v89, v89
	v_fma_f32 v92, v93, s94, s94
	v_rcp_f32_e32 v92, v92
	v_mul_f32_e32 v81, v80, v81
	v_mul_f32_e32 v80, v90, v89
	v_mul_f32_e32 v82, v80, v82
	v_mul_f32_e32 v80, v91, v92
	v_mul_f32_e32 v83, v80, v83
	v_mov_b32_e32 v80, v84
	v_mov_b32_e32 v84, v85
	v_mov_b32_e32 v85, v86
	v_med3_f32 v86, v80, s74, v145
	v_med3_f32 v84, v84, s74, v145
	v_cvt_pk_fp8_f32 v80, v86, v84
	v_med3_f32 v85, v85, s74, v145
	v_med3_f32 v84, v87, s74, v145
	v_cvt_pk_fp8_f32 v80, v85, v84 op_sel:[0,0,1]
	v_med3_f32 v84, v88, s74, v145
	v_med3_f32 v85, v81, s74, v145
	v_cvt_pk_fp8_f32 v81, v84, v85
	v_mul_f32_e32 v84, 0xbfb8aa3b, v76
	v_exp_f32_e32 v84, v84
	v_mul_f32_e32 v85, 0xbfb8aa3b, v77
	v_exp_f32_e32 v85, v85
	v_fma_f32 v84, v84, s94, s94
	v_med3_f32 v82, v82, s74, v145
	v_med3_f32 v83, v83, s74, v145
	v_rcp_f32_e32 v84, v84
	v_fma_f32 v85, v85, s94, s94
	v_cvt_pk_fp8_f32 v81, v82, v83 op_sel:[0,0,1]
	v_or_b32_e32 v82, 32, v130
	v_rcp_f32_e32 v85, v85
	v_ashrrev_i32_e32 v83, 31, v82
	v_lshlrev_b64 v[82:83], 11, v[82:83]
	v_lshl_add_u64 v[82:83], s[10:11], 0, v[82:83]
	v_mul_f32_e32 v76, v76, v84
	v_lshl_add_u64 v[82:83], v[82:83], 0, v[132:133]
	v_mul_f32_e32 v68, v76, v68
	v_mul_f32_e32 v76, v77, v85
	v_mul_f32_e32 v77, 0xbfb8aa3b, v78
	global_store_dwordx2 v[82:83], v[80:81], off
	v_exp_f32_e32 v77, v77
	v_mul_f32_e32 v80, 0xbfb8aa3b, v79
	v_exp_f32_e32 v80, v80
	v_mul_f32_e32 v69, v76, v69
	v_fma_f32 v76, v77, s94, s94
	v_rcp_f32_e32 v76, v76
	v_fma_f32 v77, v80, s94, s94
	v_mul_f32_e32 v80, 0xbfb8aa3b, v72
	v_rcp_f32_e32 v77, v77
	v_exp_f32_e32 v80, v80
	v_mul_f32_e32 v76, v78, v76
	v_mul_f32_e32 v70, v76, v70
	v_mul_f32_e32 v76, v79, v77
	v_fma_f32 v77, v80, s94, s94
	v_rcp_f32_e32 v77, v77
	v_mul_f32_e32 v78, 0xbfb8aa3b, v73
	v_exp_f32_e32 v78, v78
	v_mul_f32_e32 v71, v76, v71
	v_mul_f32_e32 v72, v72, v77
	v_mul_f32_e32 v72, v72, v64
	v_fma_f32 v64, v78, s94, s94
	v_mul_f32_e32 v76, 0xbfb8aa3b, v74
	v_rcp_f32_e32 v64, v64
	v_exp_f32_e32 v76, v76
	v_mul_f32_e32 v77, 0xbfb8aa3b, v75
	v_exp_f32_e32 v77, v77
	v_mul_f32_e32 v64, v73, v64
	v_fma_f32 v73, v76, s94, s94
	v_rcp_f32_e32 v73, v73
	v_fma_f32 v76, v77, s94, s94
	v_rcp_f32_e32 v76, v76
	v_mul_f32_e32 v65, v64, v65
	v_mul_f32_e32 v64, v74, v73
	v_mul_f32_e32 v66, v64, v66
	v_mul_f32_e32 v64, v75, v76
	v_mul_f32_e32 v67, v64, v67
	v_mov_b32_e32 v64, v68
	v_mov_b32_e32 v68, v69
	v_mov_b32_e32 v69, v70
	v_med3_f32 v70, v64, s74, v145
	v_med3_f32 v68, v68, s74, v145
	v_cvt_pk_fp8_f32 v64, v70, v68
	v_med3_f32 v69, v69, s74, v145
	v_med3_f32 v68, v71, s74, v145
	v_cvt_pk_fp8_f32 v64, v69, v68 op_sel:[0,0,1]
	v_med3_f32 v68, v72, s74, v145
	v_med3_f32 v69, v65, s74, v145
	v_cvt_pk_fp8_f32 v65, v68, v69
	v_mul_f32_e32 v68, 0xbfb8aa3b, v60
	v_exp_f32_e32 v68, v68
	v_mul_f32_e32 v69, 0xbfb8aa3b, v61
	v_exp_f32_e32 v69, v69
	v_fma_f32 v68, v68, s94, s94
	v_med3_f32 v66, v66, s74, v145
	v_med3_f32 v67, v67, s74, v145
	v_rcp_f32_e32 v68, v68
	v_fma_f32 v69, v69, s94, s94
	v_cvt_pk_fp8_f32 v65, v66, v67 op_sel:[0,0,1]
	v_or_b32_e32 v66, 48, v130
	v_rcp_f32_e32 v69, v69
	v_ashrrev_i32_e32 v67, 31, v66
	v_lshlrev_b64 v[66:67], 11, v[66:67]
	v_lshl_add_u64 v[66:67], s[10:11], 0, v[66:67]
	v_mul_f32_e32 v60, v60, v68
	v_lshl_add_u64 v[66:67], v[66:67], 0, v[132:133]
	v_mul_f32_e32 v52, v60, v52
	v_mul_f32_e32 v60, v61, v69
	v_mul_f32_e32 v61, 0xbfb8aa3b, v62
	global_store_dwordx2 v[66:67], v[64:65], off
	v_exp_f32_e32 v61, v61
	v_mul_f32_e32 v64, 0xbfb8aa3b, v63
	v_exp_f32_e32 v64, v64
	v_mul_f32_e32 v53, v60, v53
	v_fma_f32 v60, v61, s94, s94
	v_rcp_f32_e32 v60, v60
	v_fma_f32 v61, v64, s94, s94
	v_mul_f32_e32 v64, 0xbfb8aa3b, v56
	v_rcp_f32_e32 v61, v61
	v_exp_f32_e32 v64, v64
	v_mul_f32_e32 v60, v62, v60
	v_mul_f32_e32 v54, v60, v54
	v_mul_f32_e32 v60, v63, v61
	v_fma_f32 v61, v64, s94, s94
	v_rcp_f32_e32 v61, v61
	v_mul_f32_e32 v62, 0xbfb8aa3b, v57
	v_exp_f32_e32 v62, v62
	v_mul_f32_e32 v55, v60, v55
	v_mul_f32_e32 v56, v56, v61
	v_mul_f32_e32 v56, v56, v48
	v_fma_f32 v48, v62, s94, s94
	v_mul_f32_e32 v60, 0xbfb8aa3b, v58
	v_rcp_f32_e32 v48, v48
	v_exp_f32_e32 v60, v60
	v_mul_f32_e32 v61, 0xbfb8aa3b, v59
	v_exp_f32_e32 v61, v61
	v_mul_f32_e32 v48, v57, v48
	v_fma_f32 v57, v60, s94, s94
	v_rcp_f32_e32 v57, v57
	v_fma_f32 v60, v61, s94, s94
	v_rcp_f32_e32 v60, v60
	v_mul_f32_e32 v49, v48, v49
	v_mul_f32_e32 v48, v58, v57
	v_mul_f32_e32 v50, v48, v50
	v_mul_f32_e32 v48, v59, v60
	v_mul_f32_e32 v51, v48, v51
	v_mov_b32_e32 v48, v52
	v_mov_b32_e32 v52, v53
	v_mov_b32_e32 v53, v54
	v_med3_f32 v54, v48, s74, v145
	v_med3_f32 v52, v52, s74, v145
	v_cvt_pk_fp8_f32 v48, v54, v52
	v_med3_f32 v53, v53, s74, v145
	v_med3_f32 v52, v55, s74, v145
	v_cvt_pk_fp8_f32 v48, v53, v52 op_sel:[0,0,1]
	v_med3_f32 v52, v56, s74, v145
	v_med3_f32 v53, v49, s74, v145
	v_cvt_pk_fp8_f32 v49, v52, v53
	v_med3_f32 v50, v50, s74, v145
	v_med3_f32 v51, v51, s74, v145
	v_cvt_pk_fp8_f32 v49, v50, v51 op_sel:[0,0,1]
	v_mul_f32_e32 v50, 0xbfb8aa3b, v44
	v_exp_f32_e32 v52, v50
	v_mul_f32_e32 v50, 0xbfb8aa3b, v45
	v_exp_f32_e32 v53, v50
	v_add_co_u32_e32 v50, vcc, s75, v112
	v_fma_f32 v52, v52, s94, s94
	v_rcp_f32_e32 v52, v52
	v_fma_f32 v53, v53, s94, s94
	v_rcp_f32_e32 v53, v53
	v_addc_co_u32_e32 v51, vcc, 0, v113, vcc
	v_mul_f32_e32 v44, v44, v52
	v_mul_f32_e32 v36, v44, v36
	v_mul_f32_e32 v44, v45, v53
; DI int lane_fresh() { int l; asm volatile("v_mbcnt_lo_u32_b32 %0, -1, 0\n\tv_mbcnt_hi_u32_b32 %0, -1, %0" : "=v"(l)); return l; }
; #define PG8_BAR __builtin_amdgcn_s_barrier()
;     ...
;         if constexpr (ALIGN_EPI) { if (wr == 0) PG8_BAR; }
;         { const int le_ = lane_fresh(); E(acc, cur, wr, wc, le_ & 15, le_ >> 4); }
;         if (!has_next) break;
; #pragma unroll
;         for (int a = 0; a < 2; ++a)
; #pragma unroll
;             for (int b = 0; b < 2; ++b)
; #pragma unroll
;                 for (int m = 0; m < 4; ++m)
; #pragma unroll
;                     for (int n = 0; n < 2; ++n) acc[a][b][m][n] = (f32x4){0.f, 0.f, 0.f, 0.f};
;         cur = nxt; cA = nA; cB = nB; ++ui;
;         if constexpr (ALIGN_EPI) { if (wr == 1) PG8_BAR; }
	v_mul_f32_e32 v45, 0xbfb8aa3b, v46
	global_store_dwordx2 v[50:51], v[48:49], off
	v_exp_f32_e32 v45, v45
	v_mul_f32_e32 v48, 0xbfb8aa3b, v47
	v_exp_f32_e32 v48, v48
	v_mul_f32_e32 v37, v44, v37
	v_fma_f32 v44, v45, s94, s94
	v_rcp_f32_e32 v44, v44
	v_fma_f32 v45, v48, s94, s94
	v_mul_f32_e32 v48, 0xbfb8aa3b, v40
	v_rcp_f32_e32 v45, v45
	v_exp_f32_e32 v48, v48
	v_mul_f32_e32 v44, v46, v44
	v_mul_f32_e32 v38, v44, v38
	v_mul_f32_e32 v44, v47, v45
	v_fma_f32 v45, v48, s94, s94
	v_rcp_f32_e32 v45, v45
	v_mul_f32_e32 v46, 0xbfb8aa3b, v41
	v_exp_f32_e32 v46, v46
	v_mul_f32_e32 v39, v44, v39
	v_mul_f32_e32 v40, v40, v45
	v_mul_f32_e32 v40, v40, v32
	v_fma_f32 v32, v46, s94, s94
	v_mul_f32_e32 v44, 0xbfb8aa3b, v42
	v_rcp_f32_e32 v32, v32
	v_exp_f32_e32 v44, v44
	v_mul_f32_e32 v45, 0xbfb8aa3b, v43
	v_exp_f32_e32 v45, v45
	v_mul_f32_e32 v32, v41, v32
	v_fma_f32 v41, v44, s94, s94
	v_rcp_f32_e32 v41, v41
	v_fma_f32 v44, v45, s94, s94
	v_rcp_f32_e32 v44, v44
	v_mul_f32_e32 v33, v32, v33
	v_mul_f32_e32 v32, v42, v41
	v_mul_f32_e32 v34, v32, v34
	v_mul_f32_e32 v32, v43, v44
	v_mul_f32_e32 v35, v32, v35
	v_mov_b32_e32 v32, v36
	v_mov_b32_e32 v36, v37
	v_mov_b32_e32 v37, v38
	v_med3_f32 v38, v32, s74, v145
	v_med3_f32 v36, v36, s74, v145
	v_cvt_pk_fp8_f32 v32, v38, v36
	v_med3_f32 v37, v37, s74, v145
	v_med3_f32 v36, v39, s74, v145
	v_cvt_pk_fp8_f32 v32, v37, v36 op_sel:[0,0,1]
	v_med3_f32 v36, v40, s74, v145
	v_med3_f32 v37, v33, s74, v145
	v_cvt_pk_fp8_f32 v33, v36, v37
	v_med3_f32 v34, v34, s74, v145
	v_med3_f32 v35, v35, s74, v145
	v_cvt_pk_fp8_f32 v33, v34, v35 op_sel:[0,0,1]
	v_mul_f32_e32 v34, 0xbfb8aa3b, v28
	v_exp_f32_e32 v36, v34
	v_mul_f32_e32 v34, 0xbfb8aa3b, v29
	v_exp_f32_e32 v37, v34
	v_add_co_u32_e32 v34, vcc, s76, v112
	v_fma_f32 v36, v36, s94, s94
	v_rcp_f32_e32 v36, v36
	v_fma_f32 v37, v37, s94, s94
	v_rcp_f32_e32 v37, v37
	v_addc_co_u32_e32 v35, vcc, 0, v113, vcc
	v_mul_f32_e32 v28, v28, v36
	v_mul_f32_e32 v20, v28, v20
	v_mul_f32_e32 v28, v29, v37
	v_mul_f32_e32 v29, 0xbfb8aa3b, v30
	global_store_dwordx2 v[34:35], v[32:33], off
	v_exp_f32_e32 v29, v29
	v_mul_f32_e32 v32, 0xbfb8aa3b, v31
	v_exp_f32_e32 v32, v32
	v_mul_f32_e32 v21, v28, v21
	v_fma_f32 v28, v29, s94, s94
	v_rcp_f32_e32 v28, v28
	v_fma_f32 v29, v32, s94, s94
	v_mul_f32_e32 v32, 0xbfb8aa3b, v24
	v_rcp_f32_e32 v29, v29
	v_exp_f32_e32 v32, v32
	v_mul_f32_e32 v28, v30, v28
	v_mul_f32_e32 v22, v28, v22
	v_mul_f32_e32 v28, v31, v29
	v_fma_f32 v29, v32, s94, s94
	v_rcp_f32_e32 v29, v29
	v_mul_f32_e32 v30, 0xbfb8aa3b, v25
	v_exp_f32_e32 v30, v30
	v_mul_f32_e32 v23, v28, v23
	v_mul_f32_e32 v24, v24, v29
	v_mul_f32_e32 v24, v24, v16
	v_fma_f32 v16, v30, s94, s94
	v_mul_f32_e32 v28, 0xbfb8aa3b, v26
	v_rcp_f32_e32 v16, v16
	v_exp_f32_e32 v28, v28
	v_mul_f32_e32 v29, 0xbfb8aa3b, v27
	v_exp_f32_e32 v29, v29
	v_mul_f32_e32 v16, v25, v16
	v_fma_f32 v25, v28, s94, s94
	v_rcp_f32_e32 v25, v25
	v_fma_f32 v28, v29, s94, s94
	v_rcp_f32_e32 v28, v28
	v_mul_f32_e32 v17, v16, v17
	v_mul_f32_e32 v16, v26, v25
	v_mul_f32_e32 v18, v16, v18
	v_mul_f32_e32 v16, v27, v28
	v_mul_f32_e32 v19, v16, v19
	v_mov_b32_e32 v16, v20
	v_mov_b32_e32 v20, v21
	v_mov_b32_e32 v21, v22
	v_med3_f32 v22, v16, s74, v145
	v_med3_f32 v20, v20, s74, v145
	v_cvt_pk_fp8_f32 v16, v22, v20
	v_med3_f32 v21, v21, s74, v145
	v_med3_f32 v20, v23, s74, v145
	v_cvt_pk_fp8_f32 v16, v21, v20 op_sel:[0,0,1]
	v_med3_f32 v20, v24, s74, v145
	v_med3_f32 v21, v17, s74, v145
	v_cvt_pk_fp8_f32 v17, v20, v21
	v_med3_f32 v18, v18, s74, v145
	v_med3_f32 v19, v19, s74, v145
	v_cvt_pk_fp8_f32 v17, v18, v19 op_sel:[0,0,1]
	v_mul_f32_e32 v18, 0xbfb8aa3b, v12
	v_exp_f32_e32 v20, v18
	v_mul_f32_e32 v18, 0xbfb8aa3b, v13
	v_exp_f32_e32 v21, v18
	v_add_co_u32_e32 v18, vcc, s77, v112
	v_fma_f32 v20, v20, s94, s94
	v_rcp_f32_e32 v20, v20
	v_fma_f32 v21, v21, s94, s94
	v_rcp_f32_e32 v21, v21
	v_addc_co_u32_e32 v19, vcc, 0, v113, vcc
	v_mul_f32_e32 v12, v12, v20
	v_mul_f32_e32 v4, v12, v4
	v_mul_f32_e32 v12, v13, v21
	v_mul_f32_e32 v13, 0xbfb8aa3b, v14
	global_store_dwordx2 v[18:19], v[16:17], off
	v_exp_f32_e32 v13, v13
	v_mul_f32_e32 v16, 0xbfb8aa3b, v15
	v_exp_f32_e32 v16, v16
	v_mul_f32_e32 v5, v12, v5
	v_fma_f32 v12, v13, s94, s94
	v_rcp_f32_e32 v12, v12
	v_fma_f32 v13, v16, s94, s94
	v_mul_f32_e32 v16, 0xbfb8aa3b, v8
	v_rcp_f32_e32 v13, v13
	v_exp_f32_e32 v16, v16
	v_mul_f32_e32 v12, v14, v12
	v_mul_f32_e32 v6, v12, v6
	v_mul_f32_e32 v12, v15, v13
	v_fma_f32 v13, v16, s94, s94
	v_rcp_f32_e32 v13, v13
	v_mul_f32_e32 v14, 0xbfb8aa3b, v9
	v_exp_f32_e32 v14, v14
	v_mul_f32_e32 v7, v12, v7
	v_mul_f32_e32 v8, v8, v13
	v_mul_f32_e32 v8, v8, v0
	v_fma_f32 v0, v14, s94, s94
	v_mul_f32_e32 v12, 0xbfb8aa3b, v10
	v_rcp_f32_e32 v0, v0
	v_exp_f32_e32 v12, v12
	v_mul_f32_e32 v13, 0xbfb8aa3b, v11
	v_exp_f32_e32 v13, v13
	v_mul_f32_e32 v0, v9, v0
	v_fma_f32 v9, v12, s94, s94
	v_rcp_f32_e32 v9, v9
	v_fma_f32 v12, v13, s94, s94
	v_rcp_f32_e32 v12, v12
	v_mul_f32_e32 v1, v0, v1
	v_mul_f32_e32 v0, v10, v9
	v_mul_f32_e32 v2, v0, v2
	v_mul_f32_e32 v0, v11, v12
	v_mul_f32_e32 v3, v0, v3
	v_mov_b32_e32 v0, v4
	v_mov_b32_e32 v4, v5
	v_mov_b32_e32 v5, v6
	v_med3_f32 v6, v0, s74, v145
	v_med3_f32 v4, v4, s74, v145
	v_cvt_pk_fp8_f32 v0, v6, v4
	v_med3_f32 v5, v5, s74, v145
	v_med3_f32 v4, v7, s74, v145
	v_cvt_pk_fp8_f32 v0, v5, v4 op_sel:[0,0,1]
	v_med3_f32 v4, v8, s74, v145
	v_med3_f32 v5, v1, s74, v145
	v_cvt_pk_fp8_f32 v1, v4, v5
	v_med3_f32 v2, v2, s74, v145
	v_med3_f32 v3, v3, s74, v145
	v_cvt_pk_fp8_f32 v1, v2, v3 op_sel:[0,0,1]
	v_add_co_u32_e32 v2, vcc, 0x58000, v112
	s_nop 1
	v_addc_co_u32_e32 v3, vcc, 0, v113, vcc
	s_and_b64 vcc, exec, s[2:3]
	s_mov_b64 s[2:3], -1
	global_store_dwordx2 v[2:3], v[0:1], off
	s_cbranch_vccnz .LBB4_1441
	s_andn2_b64 vcc, exec, s[8:9]
	s_cbranch_vccnz .LBB4_1440
	s_barrier
	s_branch .LBB4_1440

; #define PG8_STAGE(bufoff, gbase, voff) do { const char* sb_ = (gbase); _Pragma("unroll") for (int _i = 0; _i < 2; ++_i) PG8_GLDS(sb_, (voff)[_i], bufoff, _i); } while (0)
; #define PG8_LDA(dst, b, h) do { if constexpr (F8) { _Pragma("unroll") for (int m = 0; m < 4; ++m) dst##8[m] = PG8_RD8(lds + PG8_SA(b, h) + aoff + m * 2048); } else { \
;         _Pragma("unroll") for (int m = 0; m < 4; ++m) _Pragma("unroll") for (int k = 0; k < 2; ++k) dst[m][k] = *(const PG8_LAS bf16x8*)(lds + PG8_SA(b, h) + aoff + m * 2048 + k * 1024); } } while (0)
; #define PG8_LDB(dst, b, h) do { if constexpr (F8) { _Pragma("unroll") for (int n = 0; n < 2; ++n) dst##8[n] = PG8_RD8(lds + PG8_SB(b, h) + boff + n * 2048); } else { \
;         _Pragma("unroll") for (int n = 0; n < 2; ++n) _Pragma("unroll") for (int k = 0; k < 2; ++k) dst[n][k] = *(const PG8_LAS bf16x8*)(lds + PG8_SB(b, h) + boff + n * 2048 + k * 1024); } } while (0)
; #define PG8_WAIT_V(n) asm volatile("s_waitcnt vmcnt(" #n ")" ::: "memory")
; #define PG8_WAIT_L(n) asm volatile("s_waitcnt lgkmcnt(" #n ")" ::: "memory")
; #define PG8_BAR __builtin_amdgcn_s_barrier()
; #define PG8_SCHED __builtin_amdgcn_sched_barrier(0)
;     ...
;             PG8_LDB(B0, 0, 0); PG8_LDB(B1, 0, 1); PG8_SCHED; PG8_LDA(At, 0, 0); PG8_STAGE_A(PG8_SA(1, 1), 1, k1, false);
;             PG8_WAIT_V(8); PG8_WAIT_L(0); PG8_BAR; PG8_MMA(0, 0, At, B0); PG8_MMA(0, 1, At, B1); PG8_BAR; PG8_SCHED;
;             PG8_LDA(At, 0, 1); PG8_STAGE(PG8_SB(0, 0), b2, voffB); PG8_STAGE(PG8_SB(0, 1), b2 + hstep, voffB); PG8_STAGE_A(PG8_SA(0, 0), 0, k2, last);
;             PG8_WAIT_V(8); PG8_WAIT_L(0); PG8_BAR; PG8_MMA(1, 0, At, B0); PG8_MMA(1, 1, At, B1); PG8_BAR; PG8_SCHED;
.LBB4_1541:
	ds_read_b128 v[130:133], v146
	ds_read_b128 v[134:137], v146 offset:16
	ds_read_b128 v[154:157], v146 offset:2048
	ds_read_b128 v[158:161], v146 offset:2064
	ds_read_b128 v[162:165], v147
	ds_read_b128 v[166:169], v147 offset:16
	ds_read_b128 v[170:173], v147 offset:2048
	ds_read_b128 v[174:177], v147 offset:2064
	s_add_i32 s25, s40, 0xfffc0080
	s_add_u32 s42, s38, s40
	s_addc_u32 s43, s39, s41
	s_add_u32 s42, s42, 0xfffc0080
	s_addc_u32 s43, s43, -1
	s_add_u32 s54, s36, s40
	s_addc_u32 s55, s37, s41
	s_cmp_eq_u32 s23, 12
	s_cselect_b32 s25, 0, s25
	s_cselect_b32 s43, s31, s43
	s_cselect_b32 s42, s30, s42
	ds_read_b128 v[178:181], v148
	ds_read_b128 v[182:185], v148 offset:16
	ds_read_b128 v[186:189], v148 offset:2048
	ds_read_b128 v[190:193], v148 offset:2064
	ds_read_b128 v[194:197], v148 offset:4096
	ds_read_b128 v[198:201], v148 offset:4112
	ds_read_b128 v[202:205], v148 offset:6144
	ds_read_b128 v[206:209], v148 offset:6160
	s_mov_b32 m0, s80
	s_nop 0
	global_load_lds_dwordx4 v142, s[54:55]
	s_nop 0
	s_mov_b32 m0, s86
	s_nop 0
	global_load_lds_dwordx4 v144, s[54:55]
	s_waitcnt vmcnt(8)
	s_waitcnt lgkmcnt(0)
	s_barrier
	s_setprio 1
	v_mfma_scale_f32_16x16x128_f8f6f4 v[124:127], v[130:137], v[178:185], v[124:127], v150, v149 op_sel_hi:[0,0,0]
	v_mfma_scale_f32_16x16x128_f8f6f4 v[120:123], v[154:161], v[178:185], v[120:123], v150, v149 op_sel_hi:[0,0,0]
	v_mfma_scale_f32_16x16x128_f8f6f4 v[108:111], v[130:137], v[186:193], v[108:111], v150, v149 op_sel_hi:[0,0,0]
	v_mfma_scale_f32_16x16x128_f8f6f4 v[104:107], v[154:161], v[186:193], v[104:107], v150, v149 op_sel_hi:[0,0,0]
	v_mfma_scale_f32_16x16x128_f8f6f4 v[138:141], v[130:137], v[194:201], v[92:95], v150, v149 op_sel_hi:[0,0,0]
	v_mfma_scale_f32_16x16x128_f8f6f4 v[210:213], v[154:161], v[194:201], v[88:91], v150, v149 op_sel_hi:[0,0,0]
	v_mfma_scale_f32_16x16x128_f8f6f4 v[214:217], v[130:137], v[202:209], v[76:79], v150, v149 op_sel_hi:[0,0,0]
	v_mfma_scale_f32_16x16x128_f8f6f4 v[218:221], v[154:161], v[202:209], v[72:75], v150, v149 op_sel_hi:[0,0,0]
	s_setprio 0
	s_setprio 1
	v_mfma_scale_f32_16x16x128_f8f6f4 v[116:119], v[162:169], v[178:185], v[116:119], v150, v149 op_sel_hi:[0,0,0]
	v_mfma_scale_f32_16x16x128_f8f6f4 v[112:115], v[170:177], v[178:185], v[112:115], v150, v149 op_sel_hi:[0,0,0]
	v_mfma_scale_f32_16x16x128_f8f6f4 v[100:103], v[162:169], v[186:193], v[100:103], v150, v149 op_sel_hi:[0,0,0]
	v_mfma_scale_f32_16x16x128_f8f6f4 v[96:99], v[170:177], v[186:193], v[96:99], v150, v149 op_sel_hi:[0,0,0]
	v_mfma_scale_f32_16x16x128_f8f6f4 v[178:181], v[162:169], v[194:201], v[84:87], v150, v149 op_sel_hi:[0,0,0]
	v_mfma_scale_f32_16x16x128_f8f6f4 v[182:185], v[170:177], v[194:201], v[80:83], v150, v149 op_sel_hi:[0,0,0]
	v_mfma_scale_f32_16x16x128_f8f6f4 v[186:189], v[162:169], v[202:209], v[68:71], v150, v149 op_sel_hi:[0,0,0]
	v_mfma_scale_f32_16x16x128_f8f6f4 v[190:193], v[170:177], v[202:209], v[64:67], v150, v149 op_sel_hi:[0,0,0]
	s_setprio 0
	s_barrier
	s_nop 4
	ds_read_b128 v[64:67], v148 offset:16384
	ds_read_b128 v[68:71], v148 offset:16400
	ds_read_b128 v[72:75], v148 offset:18432
	ds_read_b128 v[76:79], v148 offset:18448
	ds_read_b128 v[80:83], v148 offset:20480
	ds_read_b128 v[84:87], v148 offset:20496
	ds_read_b128 v[88:91], v148 offset:22528
	ds_read_b128 v[92:95], v148 offset:22544
	s_mov_b32 m0, s35
	s_nop 0
	global_load_lds_dwordx4 v143, s[42:43]
	s_cselect_b32 s89, s29, s37
	s_mov_b32 m0, s61
	s_nop 0
	global_load_lds_dwordx4 v145, s[42:43]
	s_cselect_b32 s90, s28, s36
	s_add_u32 s54, s42, 0x40000
	s_addc_u32 s55, s43, 0
	s_mov_b32 m0, s62
	s_nop 0
	global_load_lds_dwordx4 v143, s[54:55]
	s_nop 0
	s_mov_b32 m0, s63
	s_nop 0
	global_load_lds_dwordx4 v145, s[54:55]
	s_add_u32 s54, s90, s25
	s_addc_u32 s55, s89, 0
	s_mov_b32 m0, s60
	s_nop 0
	global_load_lds_dwordx4 v142, s[54:55]
	s_nop 0
	s_mov_b32 m0, s64
	s_nop 0
	global_load_lds_dwordx4 v144, s[54:55]
	s_waitcnt vmcnt(8)
	s_waitcnt lgkmcnt(0)
	s_barrier
	s_setprio 1
	v_mfma_scale_f32_16x16x128_f8f6f4 v[60:63], v[130:137], v[64:71], v[60:63], v150, v149 op_sel_hi:[0,0,0]
	v_mfma_scale_f32_16x16x128_f8f6f4 v[56:59], v[154:161], v[64:71], v[56:59], v150, v149 op_sel_hi:[0,0,0]
	v_mfma_scale_f32_16x16x128_f8f6f4 v[194:197], v[130:137], v[72:79], v[44:47], v150, v149 op_sel_hi:[0,0,0]
	v_mfma_scale_f32_16x16x128_f8f6f4 v[198:201], v[154:161], v[72:79], v[40:43], v150, v149 op_sel_hi:[0,0,0]
	v_mfma_scale_f32_16x16x128_f8f6f4 v[202:205], v[130:137], v[80:87], v[28:31], v150, v149 op_sel_hi:[0,0,0]
	v_mfma_scale_f32_16x16x128_f8f6f4 v[206:209], v[154:161], v[80:87], v[24:27], v150, v149 op_sel_hi:[0,0,0]
	v_mfma_scale_f32_16x16x128_f8f6f4 v[222:225], v[130:137], v[88:95], v[12:15], v150, v149 op_sel_hi:[0,0,0]
	v_mfma_scale_f32_16x16x128_f8f6f4 v[226:229], v[154:161], v[88:95], v[8:11], v150, v149 op_sel_hi:[0,0,0]
	s_setprio 0
	s_setprio 1
	v_mfma_scale_f32_16x16x128_f8f6f4 v[52:55], v[162:169], v[64:71], v[52:55], v150, v149 op_sel_hi:[0,0,0]
	v_mfma_scale_f32_16x16x128_f8f6f4 v[48:51], v[170:177], v[64:71], v[48:51], v150, v149 op_sel_hi:[0,0,0]
	v_mfma_scale_f32_16x16x128_f8f6f4 v[230:233], v[162:169], v[72:79], v[36:39], v150, v149 op_sel_hi:[0,0,0]
	v_mfma_scale_f32_16x16x128_f8f6f4 v[234:237], v[170:177], v[72:79], v[32:35], v150, v149 op_sel_hi:[0,0,0]
	v_mfma_scale_f32_16x16x128_f8f6f4 v[238:241], v[162:169], v[80:87], v[20:23], v150, v149 op_sel_hi:[0,0,0]
	v_mfma_scale_f32_16x16x128_f8f6f4 v[242:245], v[170:177], v[80:87], v[16:19], v150, v149 op_sel_hi:[0,0,0]
	v_mfma_scale_f32_16x16x128_f8f6f4 v[246:249], v[162:169], v[88:95], v[4:7], v150, v149 op_sel_hi:[0,0,0]
	v_mfma_scale_f32_16x16x128_f8f6f4 v[250:253], v[170:177], v[88:95], v[0:3], v150, v149 op_sel_hi:[0,0,0]
	s_setprio 0
	s_barrier
; #define PG8_STAGE(bufoff, gbase, voff) do { const char* sb_ = (gbase); _Pragma("unroll") for (int _i = 0; _i < 2; ++_i) PG8_GLDS(sb_, (voff)[_i], bufoff, _i); } while (0)
; #define PG8_LDA(dst, b, h) do { if constexpr (F8) { _Pragma("unroll") for (int m = 0; m < 4; ++m) dst##8[m] = PG8_RD8(lds + PG8_SA(b, h) + aoff + m * 2048); } else { \
;         _Pragma("unroll") for (int m = 0; m < 4; ++m) _Pragma("unroll") for (int k = 0; k < 2; ++k) dst[m][k] = *(const PG8_LAS bf16x8*)(lds + PG8_SA(b, h) + aoff + m * 2048 + k * 1024); } } while (0)
; #define PG8_LDB(dst, b, h) do { if constexpr (F8) { _Pragma("unroll") for (int n = 0; n < 2; ++n) dst##8[n] = PG8_RD8(lds + PG8_SB(b, h) + boff + n * 2048); } else { \
;         _Pragma("unroll") for (int n = 0; n < 2; ++n) _Pragma("unroll") for (int k = 0; k < 2; ++k) dst[n][k] = *(const PG8_LAS bf16x8*)(lds + PG8_SB(b, h) + boff + n * 2048 + k * 1024); } } while (0)
; #define PG8_WAIT_V(n) asm volatile("s_waitcnt vmcnt(" #n ")" ::: "memory")
; #define PG8_WAIT_L(n) asm volatile("s_waitcnt lgkmcnt(" #n ")" ::: "memory")
; #define PG8_BAR __builtin_amdgcn_s_barrier()
; #define PG8_SCHED __builtin_amdgcn_sched_barrier(0)
;     ...
;             PG8_LDB(B0, 1, 0); PG8_LDB(B1, 1, 1); PG8_SCHED; PG8_LDA(At, 1, 0); PG8_STAGE_A(PG8_SA(0, 1), 1, k2, last);
;             PG8_WAIT_V(8); PG8_WAIT_L(0); PG8_BAR; PG8_MMA(0, 0, At, B0); PG8_MMA(0, 1, At, B1); PG8_BAR; PG8_SCHED;
;             PG8_LDA(At, 1, 1); PG8_STAGE(PG8_SB(1, 0), b3, voffB); PG8_STAGE(PG8_SB(1, 1), b3 + hstep, voffB); PG8_STAGE_A(PG8_SA(1, 0), 0, k3, last);
;             PG8_WAIT_V(8); PG8_WAIT_L(0); PG8_BAR; PG8_MMA(1, 0, At, B0); PG8_MMA(1, 1, At, B1); PG8_BAR; PG8_SCHED;
;         }
	s_nop 4
	ds_read_b128 v[0:3], v151
	ds_read_b128 v[4:7], v151 offset:16
	ds_read_b128 v[16:19], v151 offset:2048
	ds_read_b128 v[20:23], v151 offset:2064
	ds_read_b128 v[130:133], v152
	ds_read_b128 v[134:137], v152 offset:16
	ds_read_b128 v[154:157], v152 offset:2048
	ds_read_b128 v[158:161], v152 offset:2064
	ds_read_b128 v[8:11], v148 offset:32768
	ds_read_b128 v[12:15], v148 offset:32784
	ds_read_b128 v[24:27], v148 offset:34816
	ds_read_b128 v[28:31], v148 offset:34832
	ds_read_b128 v[32:35], v148 offset:36864
	ds_read_b128 v[36:39], v148 offset:36880
	ds_read_b128 v[40:43], v148 offset:38912
	ds_read_b128 v[44:47], v148 offset:38928
	s_add_u32 s90, s54, 0x40000
	s_addc_u32 s91, s55, 0
	s_mov_b32 m0, s65
	s_nop 0
	global_load_lds_dwordx4 v142, s[90:91]
	s_nop 0
	s_mov_b32 m0, s66
	s_nop 0
	global_load_lds_dwordx4 v144, s[90:91]
	s_waitcnt vmcnt(8)
	s_waitcnt lgkmcnt(0)
	s_barrier
	s_setprio 1
	v_mfma_scale_f32_16x16x128_f8f6f4 v[124:127], v[0:7], v[8:15], v[124:127], v150, v149 op_sel_hi:[0,0,0]
	v_mfma_scale_f32_16x16x128_f8f6f4 v[120:123], v[16:23], v[8:15], v[120:123], v150, v149 op_sel_hi:[0,0,0]
	v_mfma_scale_f32_16x16x128_f8f6f4 v[108:111], v[0:7], v[24:31], v[108:111], v150, v149 op_sel_hi:[0,0,0]
	v_mfma_scale_f32_16x16x128_f8f6f4 v[104:107], v[16:23], v[24:31], v[104:107], v150, v149 op_sel_hi:[0,0,0]
	v_mfma_scale_f32_16x16x128_f8f6f4 v[92:95], v[0:7], v[32:39], v[138:141], v150, v149 op_sel_hi:[0,0,0]
	v_mfma_scale_f32_16x16x128_f8f6f4 v[88:91], v[16:23], v[32:39], v[210:213], v150, v149 op_sel_hi:[0,0,0]
	v_mfma_scale_f32_16x16x128_f8f6f4 v[76:79], v[0:7], v[40:47], v[214:217], v150, v149 op_sel_hi:[0,0,0]
	v_mfma_scale_f32_16x16x128_f8f6f4 v[72:75], v[16:23], v[40:47], v[218:221], v150, v149 op_sel_hi:[0,0,0]
	s_setprio 0
	s_setprio 1
	v_mfma_scale_f32_16x16x128_f8f6f4 v[116:119], v[130:137], v[8:15], v[116:119], v150, v149 op_sel_hi:[0,0,0]
	v_mfma_scale_f32_16x16x128_f8f6f4 v[112:115], v[154:161], v[8:15], v[112:115], v150, v149 op_sel_hi:[0,0,0]
	v_mfma_scale_f32_16x16x128_f8f6f4 v[100:103], v[130:137], v[24:31], v[100:103], v150, v149 op_sel_hi:[0,0,0]
	v_mfma_scale_f32_16x16x128_f8f6f4 v[96:99], v[154:161], v[24:31], v[96:99], v150, v149 op_sel_hi:[0,0,0]
	v_mfma_scale_f32_16x16x128_f8f6f4 v[84:87], v[130:137], v[32:39], v[178:181], v150, v149 op_sel_hi:[0,0,0]
	v_mfma_scale_f32_16x16x128_f8f6f4 v[80:83], v[154:161], v[32:39], v[182:185], v150, v149 op_sel_hi:[0,0,0]
	v_mfma_scale_f32_16x16x128_f8f6f4 v[68:71], v[130:137], v[40:47], v[186:189], v150, v149 op_sel_hi:[0,0,0]
	v_mfma_scale_f32_16x16x128_f8f6f4 v[64:67], v[154:161], v[40:47], v[190:193], v150, v149 op_sel_hi:[0,0,0]
	s_setprio 0
	s_barrier
	ds_read_b128 v[32:35], v148 offset:49152
	ds_read_b128 v[36:39], v148 offset:49168
	ds_read_b128 v[162:165], v148 offset:51200
	ds_read_b128 v[166:169], v148 offset:51216
	ds_read_b128 v[170:173], v148 offset:53248
	ds_read_b128 v[174:177], v148 offset:53264
	ds_read_b128 v[178:181], v148 offset:55296
	ds_read_b128 v[182:185], v148 offset:55312
	s_add_u32 s90, s42, 0x80
	s_addc_u32 s91, s43, 0
	s_mov_b32 m0, s74
	s_nop 0
	global_load_lds_dwordx4 v143, s[90:91]
	s_add_u32 s42, s42, 0x40080
	s_mov_b32 m0, s75
	s_nop 0
	global_load_lds_dwordx4 v145, s[90:91]
	s_addc_u32 s43, s43, 0
	s_mov_b32 m0, s78
	s_nop 0
	global_load_lds_dwordx4 v143, s[42:43]
	s_nop 0
	s_mov_b32 m0, s79
	s_nop 0
	global_load_lds_dwordx4 v145, s[42:43]
	s_add_u32 s42, s54, 0x80
	s_addc_u32 s43, s55, 0
	s_mov_b32 m0, s76
	s_nop 0
	global_load_lds_dwordx4 v142, s[42:43]
	s_nop 0
	s_mov_b32 m0, s77
	s_nop 0
	global_load_lds_dwordx4 v144, s[42:43]
	s_waitcnt vmcnt(8)
	s_waitcnt lgkmcnt(0)
	s_barrier
	s_setprio 1
	v_mfma_scale_f32_16x16x128_f8f6f4 v[60:63], v[0:7], v[32:39], v[60:63], v150, v149 op_sel_hi:[0,0,0]
	v_mfma_scale_f32_16x16x128_f8f6f4 v[56:59], v[16:23], v[32:39], v[56:59], v150, v149 op_sel_hi:[0,0,0]
	v_mfma_scale_f32_16x16x128_f8f6f4 v[44:47], v[0:7], v[162:169], v[194:197], v150, v149 op_sel_hi:[0,0,0]
	v_mfma_scale_f32_16x16x128_f8f6f4 v[40:43], v[16:23], v[162:169], v[198:201], v150, v149 op_sel_hi:[0,0,0]
	v_mfma_scale_f32_16x16x128_f8f6f4 v[28:31], v[0:7], v[170:177], v[202:205], v150, v149 op_sel_hi:[0,0,0]
	v_mfma_scale_f32_16x16x128_f8f6f4 v[24:27], v[16:23], v[170:177], v[206:209], v150, v149 op_sel_hi:[0,0,0]
	v_mfma_scale_f32_16x16x128_f8f6f4 v[12:15], v[0:7], v[178:185], v[222:225], v150, v149 op_sel_hi:[0,0,0]
	v_mfma_scale_f32_16x16x128_f8f6f4 v[8:11], v[16:23], v[178:185], v[226:229], v150, v149 op_sel_hi:[0,0,0]
	s_setprio 0
	s_setprio 1
	v_mfma_scale_f32_16x16x128_f8f6f4 v[52:55], v[130:137], v[32:39], v[52:55], v150, v149 op_sel_hi:[0,0,0]
	v_mfma_scale_f32_16x16x128_f8f6f4 v[48:51], v[154:161], v[32:39], v[48:51], v150, v149 op_sel_hi:[0,0,0]
	v_mfma_scale_f32_16x16x128_f8f6f4 v[36:39], v[130:137], v[162:169], v[230:233], v150, v149 op_sel_hi:[0,0,0]
	v_mfma_scale_f32_16x16x128_f8f6f4 v[32:35], v[154:161], v[162:169], v[234:237], v150, v149 op_sel_hi:[0,0,0]
	v_mfma_scale_f32_16x16x128_f8f6f4 v[20:23], v[130:137], v[170:177], v[238:241], v150, v149 op_sel_hi:[0,0,0]
	v_mfma_scale_f32_16x16x128_f8f6f4 v[16:19], v[154:161], v[170:177], v[242:245], v150, v149 op_sel_hi:[0,0,0]
	v_mfma_scale_f32_16x16x128_f8f6f4 v[4:7], v[130:137], v[178:185], v[246:249], v150, v149 op_sel_hi:[0,0,0]
	v_mfma_scale_f32_16x16x128_f8f6f4 v[0:3], v[154:161], v[178:185], v[250:253], v150, v149 op_sel_hi:[0,0,0]
	s_setprio 0
	s_add_i32 s23, s23, 2
	s_add_u32 s40, s40, 0x100
	s_addc_u32 s41, s41, 0
	s_cmp_gt_u32 s23, 13
	s_barrier
	s_cbranch_scc0 .LBB4_1541
	s_and_b64 vcc, exec, s[10:11]
	s_cbranch_vccz .LBB4_1544
	s_barrier
; DI unsigned pk4_f8(float a, float b, float c, float d) {
;     a = __builtin_amdgcn_fmed3f(a, -448.f, 448.f); b = __builtin_amdgcn_fmed3f(b, -448.f, 448.f); c = __builtin_amdgcn_fmed3f(c, -448.f, 448.f); d = __builtin_amdgcn_fmed3f(d, -448.f, 448.f);
;     int w = __builtin_amdgcn_cvt_pk_fp8_f32(a, b, 0, false); w = __builtin_amdgcn_cvt_pk_fp8_f32(c, d, w, true); return (unsigned)w; }
.LBB4_1544:
	s_lshl_b32 s4, s4, 8
	s_add_i32 s4, s4, s67
	v_mbcnt_lo_u32_b32 v130, -1, 0
	v_mbcnt_hi_u32_b32 v130, -1, v130
	v_and_or_b32 v132, v130, 15, s4
	v_ashrrev_i32_e32 v133, 31, v132
	v_lshl_add_u64 v[156:157], v[132:133], 2, s[12:13]
	global_load_dword v174, v[156:157], off
	v_or_b32_e32 v162, 16, v132
	v_ashrrev_i32_e32 v163, 31, v162
	v_or_b32_e32 v164, 32, v132
	v_or_b32_e32 v140, 48, v132
	v_lshlrev_b64 v[166:167], 11, v[132:133]
	v_lshl_add_u64 v[132:133], v[162:163], 2, s[12:13]
	global_load_dword v175, v[132:133], off
	v_ashrrev_i32_e32 v165, 31, v164
	v_ashrrev_i32_e32 v141, 31, v140
	v_lshl_add_u64 v[168:169], v[164:165], 2, s[12:13]
	v_lshl_add_u64 v[170:171], v[140:141], 2, s[12:13]
	global_load_dword v176, v[156:157], off offset:512
	global_load_dword v177, v[156:157], off offset:576
	global_load_dword v155, v[156:157], off offset:640
	s_nop 0
	global_load_dword v168, v[168:169], off
	s_nop 0
	global_load_dword v169, v[170:171], off
	global_load_dword v154, v[156:157], off offset:704
	s_lshl_b32 s4, s34, 8
	v_ashrrev_i32_e32 v130, 1, v130
	s_and_b32 s4, s4, 0x700
	v_and_b32_e32 v130, -8, v130
	s_or_b32 s4, s4, s73
	v_add_u32_e32 v130, s4, v130
	v_ashrrev_i32_e32 v131, 31, v130
	v_lshl_add_u64 v[138:139], v[166:167], 0, s[6:7]
	v_lshl_add_u64 v[136:137], v[166:167], 0, s[16:17]
	v_lshl_add_u64 v[134:135], v[166:167], 0, s[18:19]
	v_lshl_add_u64 v[132:133], v[166:167], 0, s[20:21]
	v_lshl_add_u64 v[172:173], s[14:15], 0, v[166:167]
	v_lshl_add_u64 v[156:157], v[172:173], 0, v[130:131]
	s_waitcnt vmcnt(7)
	v_mul_f32_e32 v174, 0x42800000, v174
	v_mul_f32_e32 v116, v116, v174
	v_mul_f32_e32 v117, v117, v174
	v_mul_f32_e32 v112, v112, v174
	v_mul_f32_e32 v113, v113, v174
	v_med3_f32 v116, v116, s87, v153
	v_med3_f32 v117, v117, s87, v153
	v_med3_f32 v112, v112, s87, v153
	v_med3_f32 v113, v113, s87, v153
	v_cvt_pk_fp8_f32 v160, v116, v117
	v_cvt_pk_fp8_f32 v161, v112, v113
	v_mul_f32_e32 v118, v118, v174
	v_mul_f32_e32 v119, v119, v174
	v_mul_f32_e32 v114, v114, v174
	v_mul_f32_e32 v115, v115, v174
	v_med3_f32 v118, v118, s87, v153
	v_med3_f32 v119, v119, s87, v153
	v_med3_f32 v114, v114, s87, v153
	v_med3_f32 v112, v115, s87, v153
	v_cvt_pk_fp8_f32 v160, v118, v119 op_sel:[0,0,1]
	v_cvt_pk_fp8_f32 v161, v114, v112 op_sel:[0,0,1]
	v_lshl_add_u64 v[112:113], s[46:47], 0, v[166:167]
	v_lshl_add_u64 v[112:113], v[112:113], 0, v[130:131]
	v_add_co_u32_e32 v112, vcc, s88, v112
	s_waitcnt vmcnt(6)
	v_addc_co_u32_e32 v113, vcc, 0, v113, vcc
	global_store_dwordx2 v[112:113], v[160:161], off offset:128
	v_mul_f32_e32 v175, 0x42800000, v175
	v_mul_f32_e32 v112, v104, v175
	v_mul_f32_e32 v104, v108, v175
	v_mul_f32_e32 v108, v109, v175
	v_mul_f32_e32 v109, v110, v175
	v_med3_f32 v110, v104, s87, v153
	v_med3_f32 v108, v108, s87, v153
	v_cvt_pk_fp8_f32 v104, v110, v108
	v_mul_f32_e32 v108, v111, v175
	v_med3_f32 v109, v109, s87, v153
	v_med3_f32 v108, v108, s87, v153
	v_cvt_pk_fp8_f32 v104, v109, v108 op_sel:[0,0,1]
	v_mov_b32_e32 v108, v112
	v_mul_f32_e32 v105, v105, v175
	v_med3_f32 v108, v108, s87, v153
	v_med3_f32 v109, v105, s87, v153
	v_cvt_pk_fp8_f32 v105, v108, v109
	v_mul_f32_e32 v106, v106, v175
	v_mul_f32_e32 v107, v107, v175
	v_med3_f32 v106, v106, s87, v153
	v_med3_f32 v107, v107, s87, v153
	v_cvt_pk_fp8_f32 v105, v106, v107 op_sel:[0,0,1]
	v_lshlrev_b64 v[106:107], 11, v[162:163]
	v_lshl_add_u64 v[108:109], s[14:15], 0, v[106:107]
	v_lshl_add_u64 v[108:109], v[108:109], 0, v[130:131]
	global_store_dwordx2 v[108:109], v[104:105], off
	v_mul_f32_e32 v104, v96, v175
	v_mul_f32_e32 v96, v100, v175
	v_mul_f32_e32 v100, v101, v175
	v_mul_f32_e32 v101, v102, v175
	v_med3_f32 v102, v96, s87, v153
	v_med3_f32 v100, v100, s87, v153
	v_cvt_pk_fp8_f32 v96, v102, v100
	v_mul_f32_e32 v100, v103, v175
	v_med3_f32 v101, v101, s87, v153
	v_med3_f32 v100, v100, s87, v153
	v_cvt_pk_fp8_f32 v96, v101, v100 op_sel:[0,0,1]
	v_mov_b32_e32 v100, v104
	v_mul_f32_e32 v97, v97, v175
	v_med3_f32 v100, v100, s87, v153
	v_med3_f32 v101, v97, s87, v153
	v_cvt_pk_fp8_f32 v97, v100, v101
	v_mul_f32_e32 v98, v98, v175
	v_mul_f32_e32 v99, v99, v175
	v_med3_f32 v98, v98, s87, v153
	v_med3_f32 v99, v99, s87, v153
	v_cvt_pk_fp8_f32 v97, v98, v99 op_sel:[0,0,1]
	v_lshl_add_u64 v[98:99], s[46:47], 0, v[106:107]
	v_lshl_add_u64 v[98:99], v[98:99], 0, v[130:131]
	v_add_co_u32_e32 v98, vcc, s88, v98
	s_waitcnt vmcnt(4)
	v_addc_co_u32_e32 v99, vcc, 0, v99, vcc
	global_store_dwordx2 v[98:99], v[96:97], off offset:128
	v_mul_f32_e32 v168, 0x42800000, v168
	v_mul_f32_e32 v96, v88, v168
	v_mul_f32_e32 v88, v92, v168
	v_mul_f32_e32 v92, v93, v168
	v_mul_f32_e32 v93, v94, v168
	v_med3_f32 v94, v88, s87, v153
	v_med3_f32 v92, v92, s87, v153
	v_cvt_pk_fp8_f32 v88, v94, v92
	v_mul_f32_e32 v92, v95, v168
	v_med3_f32 v93, v93, s87, v153
	v_med3_f32 v92, v92, s87, v153
	v_cvt_pk_fp8_f32 v88, v93, v92 op_sel:[0,0,1]
	v_mov_b32_e32 v92, v96
	v_mul_f32_e32 v89, v89, v168
	v_med3_f32 v92, v92, s87, v153
	v_med3_f32 v93, v89, s87, v153
	v_cvt_pk_fp8_f32 v89, v92, v93
	v_mul_f32_e32 v90, v90, v168
	v_mul_f32_e32 v91, v91, v168
	v_med3_f32 v90, v90, s87, v153
	v_med3_f32 v91, v91, s87, v153
	v_cvt_pk_fp8_f32 v89, v90, v91 op_sel:[0,0,1]
	v_lshlrev_b64 v[90:91], 11, v[164:165]
	v_lshl_add_u64 v[92:93], s[14:15], 0, v[90:91]
	v_lshl_add_u64 v[92:93], v[92:93], 0, v[130:131]
	global_store_dwordx2 v[92:93], v[88:89], off
	v_mul_f32_e32 v88, v80, v168
	v_mul_f32_e32 v80, v84, v168
	v_mul_f32_e32 v84, v85, v168
	v_mul_f32_e32 v85, v86, v168
	v_med3_f32 v86, v80, s87, v153
	v_med3_f32 v84, v84, s87, v153
	v_cvt_pk_fp8_f32 v80, v86, v84
	v_mul_f32_e32 v84, v87, v168
	v_med3_f32 v85, v85, s87, v153
	v_med3_f32 v84, v84, s87, v153
	v_cvt_pk_fp8_f32 v80, v85, v84 op_sel:[0,0,1]
	v_mov_b32_e32 v84, v88
	v_mul_f32_e32 v81, v81, v168
	v_med3_f32 v84, v84, s87, v153
	v_med3_f32 v85, v81, s87, v153
	v_cvt_pk_fp8_f32 v81, v84, v85
	v_mul_f32_e32 v82, v82, v168
	v_mul_f32_e32 v83, v83, v168
	v_med3_f32 v82, v82, s87, v153
	v_med3_f32 v83, v83, s87, v153
	v_cvt_pk_fp8_f32 v81, v82, v83 op_sel:[0,0,1]
	v_lshl_add_u64 v[82:83], s[46:47], 0, v[90:91]
	v_lshl_add_u64 v[82:83], v[82:83], 0, v[130:131]
	v_add_co_u32_e32 v82, vcc, s88, v82
	s_waitcnt vmcnt(5)
; DI unsigned pk4_f8(float a, float b, float c, float d) {
;     a = __builtin_amdgcn_fmed3f(a, -448.f, 448.f); b = __builtin_amdgcn_fmed3f(b, -448.f, 448.f); c = __builtin_amdgcn_fmed3f(c, -448.f, 448.f); d = __builtin_amdgcn_fmed3f(d, -448.f, 448.f);
;     int w = __builtin_amdgcn_cvt_pk_fp8_f32(a, b, 0, false); w = __builtin_amdgcn_cvt_pk_fp8_f32(c, d, w, true); return (unsigned)w; }
	v_addc_co_u32_e32 v83, vcc, 0, v83, vcc
	global_store_dwordx2 v[82:83], v[80:81], off offset:128
	v_mul_f32_e32 v169, 0x42800000, v169
	v_mul_f32_e32 v80, v72, v169
	v_mul_f32_e32 v72, v76, v169
	v_mul_f32_e32 v76, v77, v169
	v_mul_f32_e32 v77, v78, v169
	v_med3_f32 v78, v72, s87, v153
	v_med3_f32 v76, v76, s87, v153
	v_cvt_pk_fp8_f32 v72, v78, v76
	v_mul_f32_e32 v76, v79, v169
	v_med3_f32 v77, v77, s87, v153
	v_med3_f32 v76, v76, s87, v153
	v_cvt_pk_fp8_f32 v72, v77, v76 op_sel:[0,0,1]
	v_mov_b32_e32 v76, v80
	v_mul_f32_e32 v73, v73, v169
	v_med3_f32 v76, v76, s87, v153
	v_med3_f32 v77, v73, s87, v153
	v_cvt_pk_fp8_f32 v73, v76, v77
	v_mul_f32_e32 v74, v74, v169
	v_mul_f32_e32 v75, v75, v169
	v_med3_f32 v74, v74, s87, v153
	v_med3_f32 v75, v75, s87, v153
	v_cvt_pk_fp8_f32 v73, v74, v75 op_sel:[0,0,1]
	v_lshlrev_b64 v[74:75], 11, v[140:141]
	v_lshl_add_u64 v[76:77], s[14:15], 0, v[74:75]
	v_lshl_add_u64 v[76:77], v[76:77], 0, v[130:131]
	global_store_dwordx2 v[76:77], v[72:73], off
	v_mul_f32_e32 v72, v64, v169
	v_mul_f32_e32 v64, v68, v169
	v_mul_f32_e32 v68, v69, v169
	v_mul_f32_e32 v69, v70, v169
	v_med3_f32 v70, v64, s87, v153
	v_med3_f32 v68, v68, s87, v153
	v_cvt_pk_fp8_f32 v64, v70, v68
	v_mul_f32_e32 v68, v71, v169
	v_med3_f32 v69, v69, s87, v153
	v_med3_f32 v68, v68, s87, v153
	v_cvt_pk_fp8_f32 v64, v69, v68 op_sel:[0,0,1]
	v_mov_b32_e32 v68, v72
	v_mul_f32_e32 v65, v65, v169
	v_med3_f32 v68, v68, s87, v153
	v_med3_f32 v69, v65, s87, v153
	v_cvt_pk_fp8_f32 v65, v68, v69
	v_mul_f32_e32 v176, 0x42800000, v176
	v_mul_f32_e32 v68, v56, v176
	v_mul_f32_e32 v56, v60, v176
	v_mul_f32_e32 v60, v61, v176
	v_mul_f32_e32 v61, v62, v176
	v_med3_f32 v62, v56, s87, v153
	v_med3_f32 v60, v60, s87, v153
	v_cvt_pk_fp8_f32 v56, v62, v60
	v_mul_f32_e32 v60, v63, v176
	v_med3_f32 v61, v61, s87, v153
	v_med3_f32 v60, v60, s87, v153
	v_cvt_pk_fp8_f32 v56, v61, v60 op_sel:[0,0,1]
	v_mov_b32_e32 v60, v68
	v_mul_f32_e32 v57, v57, v176
	v_med3_f32 v60, v60, s87, v153
	v_med3_f32 v61, v57, s87, v153
	v_cvt_pk_fp8_f32 v57, v60, v61
	v_mul_f32_e32 v58, v58, v176
	v_mul_f32_e32 v59, v59, v176
	v_med3_f32 v58, v58, s87, v153
	v_med3_f32 v59, v59, s87, v153
	v_cvt_pk_fp8_f32 v57, v58, v59 op_sel:[0,0,1]
	v_lshl_add_u64 v[58:59], s[14:15], 0, v[138:139]
	v_lshl_add_u64 v[58:59], v[58:59], 0, v[130:131]
	global_store_dwordx2 v[58:59], v[56:57], off
	v_mul_f32_e32 v56, v48, v176
	v_mul_f32_e32 v48, v52, v176
	v_mul_f32_e32 v52, v53, v176
	v_mul_f32_e32 v53, v54, v176
	v_med3_f32 v54, v48, s87, v153
	v_med3_f32 v52, v52, s87, v153
	v_cvt_pk_fp8_f32 v48, v54, v52
	v_mul_f32_e32 v52, v55, v176
	v_med3_f32 v53, v53, s87, v153
	v_med3_f32 v52, v52, s87, v153
	v_cvt_pk_fp8_f32 v48, v53, v52 op_sel:[0,0,1]
	v_mov_b32_e32 v52, v56
	v_mul_f32_e32 v49, v49, v176
	v_med3_f32 v52, v52, s87, v153
	v_med3_f32 v53, v49, s87, v153
	v_cvt_pk_fp8_f32 v49, v52, v53
	v_mul_f32_e32 v177, 0x42800000, v177
	v_mul_f32_e32 v52, v40, v177
	v_mul_f32_e32 v40, v44, v177
	v_mul_f32_e32 v44, v45, v177
	v_mul_f32_e32 v45, v46, v177
	v_med3_f32 v46, v40, s87, v153
	v_med3_f32 v44, v44, s87, v153
	v_cvt_pk_fp8_f32 v40, v46, v44
	v_mul_f32_e32 v44, v47, v177
	v_med3_f32 v45, v45, s87, v153
	v_med3_f32 v44, v44, s87, v153
	v_cvt_pk_fp8_f32 v40, v45, v44 op_sel:[0,0,1]
	v_mov_b32_e32 v44, v52
	v_mul_f32_e32 v41, v41, v177
	v_med3_f32 v44, v44, s87, v153
	v_med3_f32 v45, v41, s87, v153
	v_cvt_pk_fp8_f32 v41, v44, v45
	v_mul_f32_e32 v42, v42, v177
	v_mul_f32_e32 v43, v43, v177
	v_med3_f32 v42, v42, s87, v153
	v_med3_f32 v43, v43, s87, v153
	v_cvt_pk_fp8_f32 v41, v42, v43 op_sel:[0,0,1]
	v_lshl_add_u64 v[42:43], s[14:15], 0, v[136:137]
	v_lshl_add_u64 v[42:43], v[42:43], 0, v[130:131]
	global_store_dwordx2 v[42:43], v[40:41], off
	v_mul_f32_e32 v40, v32, v177
	v_mul_f32_e32 v32, v36, v177
	v_mul_f32_e32 v36, v37, v177
	v_mul_f32_e32 v37, v38, v177
	v_med3_f32 v38, v32, s87, v153
	v_med3_f32 v36, v36, s87, v153
	v_cvt_pk_fp8_f32 v32, v38, v36
	v_mul_f32_e32 v36, v39, v177
	v_med3_f32 v37, v37, s87, v153
	v_med3_f32 v36, v36, s87, v153
	v_cvt_pk_fp8_f32 v32, v37, v36 op_sel:[0,0,1]
	v_mov_b32_e32 v36, v40
	v_mul_f32_e32 v33, v33, v177
	v_med3_f32 v36, v36, s87, v153
	v_med3_f32 v37, v33, s87, v153
	v_cvt_pk_fp8_f32 v33, v36, v37
	v_mul_f32_e32 v155, 0x42800000, v155
	v_mul_f32_e32 v36, v24, v155
	v_mul_f32_e32 v24, v28, v155
	v_mul_f32_e32 v28, v29, v155
	v_mul_f32_e32 v29, v30, v155
	v_med3_f32 v30, v24, s87, v153
	v_med3_f32 v28, v28, s87, v153
	v_cvt_pk_fp8_f32 v24, v30, v28
	v_mul_f32_e32 v28, v31, v155
	v_med3_f32 v29, v29, s87, v153
	v_med3_f32 v28, v28, s87, v153
	v_cvt_pk_fp8_f32 v24, v29, v28 op_sel:[0,0,1]
	v_mov_b32_e32 v28, v36
	v_mul_f32_e32 v25, v25, v155
	v_med3_f32 v28, v28, s87, v153
	v_med3_f32 v29, v25, s87, v153
	v_cvt_pk_fp8_f32 v25, v28, v29
	v_mul_f32_e32 v26, v26, v155
	v_mul_f32_e32 v27, v27, v155
	v_med3_f32 v26, v26, s87, v153
	v_med3_f32 v27, v27, s87, v153
	v_cvt_pk_fp8_f32 v25, v26, v27 op_sel:[0,0,1]
	v_lshl_add_u64 v[26:27], s[14:15], 0, v[134:135]
	v_lshl_add_u64 v[26:27], v[26:27], 0, v[130:131]
	global_store_dwordx2 v[26:27], v[24:25], off
	v_mul_f32_e32 v24, v16, v155
	v_mul_f32_e32 v16, v20, v155
	v_mul_f32_e32 v20, v21, v155
	v_mul_f32_e32 v21, v22, v155
	v_med3_f32 v22, v16, s87, v153
	v_med3_f32 v20, v20, s87, v153
	v_cvt_pk_fp8_f32 v16, v22, v20
	v_mul_f32_e32 v20, v23, v155
	v_med3_f32 v21, v21, s87, v153
	v_med3_f32 v20, v20, s87, v153
	v_cvt_pk_fp8_f32 v16, v21, v20 op_sel:[0,0,1]
	v_mov_b32_e32 v20, v24
	v_mul_f32_e32 v17, v17, v155
	v_med3_f32 v20, v20, s87, v153
	v_med3_f32 v21, v17, s87, v153
	s_waitcnt vmcnt(9)
; DI int lane_fresh() { int l; asm volatile("v_mbcnt_lo_u32_b32 %0, -1, 0\n\tv_mbcnt_hi_u32_b32 %0, -1, %0" : "=v"(l)); return l; }
; #define PG8_BAR __builtin_amdgcn_s_barrier()
;     ...
;         if constexpr (ALIGN_EPI) { if (wr == 0) PG8_BAR; }
;         { const int le_ = lane_fresh(); E(acc, cur, wr, wc, le_ & 15, le_ >> 4); }
;         if (!has_next) break;
; #pragma unroll
;         for (int a = 0; a < 2; ++a)
; #pragma unroll
;             for (int b = 0; b < 2; ++b)
; #pragma unroll
;                 for (int m = 0; m < 4; ++m)
; #pragma unroll
;                     for (int n = 0; n < 2; ++n) acc[a][b][m][n] = (f32x4){0.f, 0.f, 0.f, 0.f};
;         cur = nxt; cA = nA; cB = nB; ++ui;
;         if constexpr (ALIGN_EPI) { if (wr == 1) PG8_BAR; }
	v_cvt_pk_fp8_f32 v17, v20, v21
	v_mul_f32_e32 v154, 0x42800000, v154
	v_mul_f32_e32 v20, v8, v154
	v_mul_f32_e32 v8, v12, v154
	v_mul_f32_e32 v12, v13, v154
	v_mul_f32_e32 v13, v14, v154
	v_med3_f32 v14, v8, s87, v153
	v_med3_f32 v12, v12, s87, v153
	v_cvt_pk_fp8_f32 v8, v14, v12
	v_mul_f32_e32 v12, v15, v154
	v_med3_f32 v13, v13, s87, v153
	v_med3_f32 v12, v12, s87, v153
	v_cvt_pk_fp8_f32 v8, v13, v12 op_sel:[0,0,1]
	v_mov_b32_e32 v12, v20
	v_mul_f32_e32 v9, v9, v154
	v_med3_f32 v12, v12, s87, v153
	v_med3_f32 v13, v9, s87, v153
	v_cvt_pk_fp8_f32 v9, v12, v13
	v_mul_f32_e32 v10, v10, v154
	v_mul_f32_e32 v11, v11, v154
	v_med3_f32 v10, v10, s87, v153
	v_med3_f32 v11, v11, s87, v153
	v_cvt_pk_fp8_f32 v9, v10, v11 op_sel:[0,0,1]
	v_lshl_add_u64 v[10:11], s[14:15], 0, v[132:133]
	v_lshl_add_u64 v[10:11], v[10:11], 0, v[130:131]
	global_store_dwordx2 v[10:11], v[8:9], off
	v_mul_f32_e32 v8, v0, v154
	v_mul_f32_e32 v0, v4, v154
	v_mul_f32_e32 v4, v5, v154
	v_mul_f32_e32 v5, v6, v154
	v_med3_f32 v6, v0, s87, v153
	v_med3_f32 v4, v4, s87, v153
	v_mul_f32_e32 v66, v66, v169
	v_mul_f32_e32 v67, v67, v169
	v_cvt_pk_fp8_f32 v0, v6, v4
	v_med3_f32 v66, v66, s87, v153
	v_med3_f32 v67, v67, s87, v153
	v_cvt_pk_fp8_f32 v65, v66, v67 op_sel:[0,0,1]
	v_lshl_add_u64 v[66:67], s[46:47], 0, v[74:75]
	v_mul_f32_e32 v50, v50, v176
	v_mul_f32_e32 v51, v51, v176
	v_mul_f32_e32 v4, v7, v154
	v_lshl_add_u64 v[66:67], v[66:67], 0, v[130:131]
	v_med3_f32 v50, v50, s87, v153
	v_med3_f32 v51, v51, s87, v153
	v_med3_f32 v5, v5, s87, v153
	v_med3_f32 v4, v4, s87, v153
	v_add_co_u32_e32 v66, vcc, s88, v66
	v_cvt_pk_fp8_f32 v49, v50, v51 op_sel:[0,0,1]
	v_lshl_add_u64 v[50:51], s[46:47], 0, v[138:139]
	v_mul_f32_e32 v34, v34, v177
	v_mul_f32_e32 v35, v35, v177
	v_cvt_pk_fp8_f32 v0, v5, v4 op_sel:[0,0,1]
	v_mov_b32_e32 v4, v8
	v_mul_f32_e32 v1, v1, v154
	v_mul_f32_e32 v124, v124, v174
	v_mul_f32_e32 v125, v125, v174
	v_mul_f32_e32 v120, v120, v174
	v_mul_f32_e32 v121, v121, v174
	v_addc_co_u32_e32 v67, vcc, 0, v67, vcc
	v_lshl_add_u64 v[50:51], v[50:51], 0, v[130:131]
	v_med3_f32 v34, v34, s87, v153
	v_med3_f32 v35, v35, s87, v153
	v_med3_f32 v4, v4, s87, v153
	v_med3_f32 v5, v1, s87, v153
	v_med3_f32 v124, v124, s87, v153
	v_med3_f32 v125, v125, s87, v153
	v_med3_f32 v120, v120, s87, v153
	v_med3_f32 v121, v121, s87, v153
	v_add_co_u32_e32 v50, vcc, s88, v50
	v_cvt_pk_fp8_f32 v33, v34, v35 op_sel:[0,0,1]
	v_lshl_add_u64 v[34:35], s[46:47], 0, v[136:137]
	v_mul_f32_e32 v18, v18, v155
	v_mul_f32_e32 v19, v19, v155
	v_cvt_pk_fp8_f32 v1, v4, v5
	v_cvt_pk_fp8_f32 v158, v124, v125
	v_cvt_pk_fp8_f32 v159, v120, v121
	v_addc_co_u32_e32 v51, vcc, 0, v51, vcc
	v_lshl_add_u64 v[34:35], v[34:35], 0, v[130:131]
	v_med3_f32 v18, v18, s87, v153
	v_med3_f32 v19, v19, s87, v153
	v_add_co_u32_e32 v34, vcc, s88, v34
	v_cvt_pk_fp8_f32 v17, v18, v19 op_sel:[0,0,1]
	v_lshl_add_u64 v[18:19], s[46:47], 0, v[134:135]
	v_mul_f32_e32 v2, v2, v154
	v_mul_f32_e32 v3, v3, v154
	v_mul_f32_e32 v126, v126, v174
	v_mul_f32_e32 v127, v127, v174
	v_mul_f32_e32 v122, v122, v174
	v_mul_f32_e32 v123, v123, v174
	v_addc_co_u32_e32 v35, vcc, 0, v35, vcc
	v_lshl_add_u64 v[18:19], v[18:19], 0, v[130:131]
	v_med3_f32 v2, v2, s87, v153
	v_med3_f32 v3, v3, s87, v153
	v_med3_f32 v126, v126, s87, v153
	v_med3_f32 v127, v127, s87, v153
	v_med3_f32 v122, v122, s87, v153
	v_med3_f32 v123, v123, s87, v153
	v_add_co_u32_e32 v18, vcc, s88, v18
	v_cvt_pk_fp8_f32 v1, v2, v3 op_sel:[0,0,1]
	v_lshl_add_u64 v[2:3], s[46:47], 0, v[132:133]
	v_cvt_pk_fp8_f32 v158, v126, v127 op_sel:[0,0,1]
	v_cvt_pk_fp8_f32 v159, v122, v123 op_sel:[0,0,1]
	v_addc_co_u32_e32 v19, vcc, 0, v19, vcc
	v_lshl_add_u64 v[2:3], v[2:3], 0, v[130:131]
	v_add_co_u32_e32 v2, vcc, 0x2d800000, v2
	global_store_dwordx2 v[156:157], v[158:159], off
	s_nop 0
	v_addc_co_u32_e32 v3, vcc, 0, v3, vcc
	s_andn2_b64 vcc, exec, s[26:27]
	s_mov_b64 s[26:27], -1
	global_store_dwordx2 v[66:67], v[64:65], off offset:128
	global_store_dwordx2 v[50:51], v[48:49], off offset:128
	global_store_dwordx2 v[34:35], v[32:33], off offset:128
	global_store_dwordx2 v[18:19], v[16:17], off offset:128
	global_store_dwordx2 v[2:3], v[0:1], off offset:128
	s_cbranch_vccnz .LBB4_1532
	s_andn2_b64 vcc, exec, s[8:9]
	s_cbranch_vccnz .LBB4_1531
	s_barrier
	s_branch .LBB4_1531
